# tile-blocked fp8 expert-weight layout [256-row tile][k block][8 row groups][32x128B] (WG writes 32KB contiguous in P0; GEMM B tile = 32KB contiguous per K-step) + all v26 policies
# speedup vs baseline: 1.0052x; 1.0052x over previous
; __device__ __forceinline__ MoeItem moe_item(const float* wg, const float* wu, const float* wd, const float* win, const float* wout, const float* wpn, const float* wpd, unsigned char* ws, int r, int lane) {
;     ...
;     const int mat = r / MOE_IE, q = r % MOE_IE, e = mat / 3, which = mat % 3, kb = q / 64, nb = q % 64, n0 = nb * 32;
;     const float* src = (which == 0 ? wg : (which == 1 ? wu : wd)) + (size_t)e * DM * DFF + (size_t)(kb * 128 + (lane >> 5)) * DFF + n0 + (lane & 31);
;     unsigned char* dst;
;     if (which < 2) dst = ws + WS_WGUT + ((size_t)(e * 16 + (n0 >> 7)) * 256 + which * 128 + (n0 & 127)) * DM;
;     else dst = ws + WS_WDT + ((size_t)e * DM + n0) * DFF;
;     MoeItem it; it.stride = DFF; it.dpitch = DM; it.src = src; it.dst = dst + kb * 128 + (size_t)(lane >> 3) * DM + 16 * (lane & 7); return it;
;     ...
;         const int nmine = (NMOE - gw + NGW - 1) / NGW;
;         const int last = gw + (nmine - 1) * NGW;
;         MoeItem ia = moe_item(wg, wu, wd, win, wout, wpn, wpd, F.ws, gw, F.lane), ib = ia;
.LBB0_49:
	s_mov_b32 s32, 0
	s_abs_i32 s6, s72
	v_cvt_f32_u32_e32 v1, s6
	s_sub_i32 s4, s72, s3
	s_add_i32 s68, s4, 0x193ff
	s_sub_i32 s4, 0xfffe6c01, s4
	v_rcp_iflag_f32_e32 v1, v1
	s_max_i32 s7, s68, s4
	s_sub_i32 s4, 0, s6
	v_mul_f32_e32 v1, 0x4f7ffffe, v1
	v_cvt_u32_f32_e32 v1, v1
	s_nop 0
	v_readfirstlane_b32 s5, v1
	s_mul_i32 s4, s4, s5
	s_mul_hi_u32 s4, s5, s4
	s_add_i32 s5, s5, s4
	s_cmp_lt_i32 s3, 0x19000
	s_mul_hi_u32 s47, s7, s5
	s_cbranch_scc0 .LBB0_54
	s_cmp_lt_i32 s3, 0x18c00
	s_cbranch_scc0 .LBB0_56
	s_cmp_lt_i32 s3, 0x18000
	s_cbranch_scc0 .LBB0_57
	s_mov_b32 s32, 1
	s_ashr_i32 s4, s3, 31
	s_lshr_b32 s4, s4, 22
	s_add_i32 s4, s3, s4
	s_ashr_i32 s5, s4, 10
	s_and_b32 s4, s4, 0xfc00
	s_sub_i32 s38, s3, s4
	s_mul_hi_i32 s4, s3, 0x2aaaaaab
	s_lshr_b32 s39, s4, 31
	s_ashr_i32 s4, s4, 9
	s_add_i32 s4, s4, s39
	s_mul_hi_i32 s39, s5, 0x55555556
	s_lshr_b32 s42, s39, 31
	s_add_i32 s39, s39, s42
	s_mul_i32 s39, s39, 3
	s_sub_i32 s69, s5, s39
	s_sext_i32_i16 s5, s38
	s_bfe_u32 s5, s5, 0x60019
	s_add_i32 s42, s38, s5
	s_and_b32 s5, s42, 0xffc0
	s_sub_i32 s5, s38, s5
	s_sext_i32_i16 s70, s5
	s_lshl_b32 s38, s70, 5
	s_ashr_i32 s5, s4, 31
	s_ashr_i32 s39, s38, 31
	s_cmp_gt_i32 s69, 1
	s_sext_i32_i16 s71, s42
	s_cbranch_scc0 .LBB0_58
	s_lshl_b64 s[42:43], s[4:5], 22
	s_lshl_b64 s[44:45], s[38:39], 11
	s_lshr_b32 s99, s44, 4
	s_and_b32 s99, s99, 0x7000
	s_and_b32 s44, s44, 0xfff80000
	s_or_b32 s44, s44, s99
	s_add_u32 s42, s82, s42
	s_addc_u32 s43, s83, s43
	s_add_u32 s42, s42, s44
	s_addc_u32 s43, s43, s45
	s_add_u32 s42, s42, 0x24000000
	s_addc_u32 s43, s43, 0
	s_mov_b64 s[44:45], 0
	s_branch .LBB0_59

; __device__ __forceinline__ MoeItem moe_item(const float* wg, const float* wu, const float* wd, const float* win, const float* wout, const float* wpn, const float* wpd, unsigned char* ws, int r, int lane) {
;     ...
;     const int mat = r / MOE_IE, q = r % MOE_IE, e = mat / 3, which = mat % 3, kb = q / 64, nb = q % 64, n0 = nb * 32;
;     const float* src = (which == 0 ? wg : (which == 1 ? wu : wd)) + (size_t)e * DM * DFF + (size_t)(kb * 128 + (lane >> 5)) * DFF + n0 + (lane & 31);
;     unsigned char* dst;
;     if (which < 2) dst = ws + WS_WGUT + ((size_t)(e * 16 + (n0 >> 7)) * 256 + which * 128 + (n0 & 127)) * DM;
;     else dst = ws + WS_WDT + ((size_t)e * DM + n0) * DFF;
;     MoeItem it; it.stride = DFF; it.dpitch = DM; it.src = src; it.dst = dst + kb * 128 + (size_t)(lane >> 3) * DM + 16 * (lane & 7); return it;
.LBB0_59:
	s_andn2_b64 vcc, exec, s[44:45]
	s_lshr_b32 s44, s71, 6
	s_cbranch_vccnz .LBB0_61
	s_lshl_b32 s42, s4, 4
	s_ashr_i32 s43, s70, 2
	s_add_i32 s42, s43, s42
	s_ashr_i32 s43, s42, 31
	s_lshl_b32 s45, s69, 7
	s_lshl_b64 s[42:43], s[42:43], 8
	s_ashr_i32 s70, s45, 31
	s_add_u32 s42, s42, s45
	s_addc_u32 s43, s43, s70
	s_and_b32 s45, s38, 0x60
	s_or_b32 s42, s42, s45
	s_lshl_b64 s[42:43], s[42:43], 11
	s_lshr_b32 s99, s42, 4
	s_and_b32 s99, s99, 0x7000
	s_and_b32 s42, s42, 0xfff80000
	s_or_b32 s42, s42, s99
	s_add_u32 s42, s82, s42
	s_addc_u32 s43, s83, s43
	s_add_u32 s42, s42, 0x4000000
	s_addc_u32 s43, s43, 0
.LBB0_61:
	s_cmp_eq_u32 s69, 1
	s_cselect_b32 s45, s20, s24
	s_cselect_b32 s70, s21, s25
	s_cmp_eq_u32 s69, 0
	s_cselect_b32 s69, s17, s70
	s_cselect_b32 s45, s16, s45
	s_lshl_b64 s[4:5], s[4:5], 24
	s_sext_i32_i16 s44, s44
	s_add_u32 s4, s45, s4
	s_addc_u32 s5, s69, s5
	s_lshl_b32 s44, s44, 7
	v_lshrrev_b32_e32 v1, 5, v170
	v_or_b32_e32 v4, s44, v1
	v_ashrrev_i32_e32 v5, 31, v4
	v_lshlrev_b64 v[4:5], 13, v[4:5]
	v_lshl_add_u64 v[4:5], s[4:5], 0, v[4:5]
	s_ashr_i32 s4, s44, 31
	v_lshl_add_u64 v[4:5], s[38:39], 2, v[4:5]
	v_and_b32_e32 v1, 31, v0
	s_lshl_b32 s98, s44, 8
	s_add_u32 s38, s42, s98
	v_lshlrev_b32_e32 v6, 2, v1
	v_mov_b32_e32 v7, 0
	s_addc_u32 s39, s43, s4
	v_lshl_add_u64 v[4:5], v[4:5], 0, v[6:7]
	v_mov_b64_e32 v[6:7], s[38:39]
	s_mov_b64 s[44:45], 0x800
	s_branch .LBB0_73

; #define MOE_LOAD(v, it) do { _Pragma("unroll") for (int i_ = 0; i_ < 64; ++i_) v[i_] = __builtin_nontemporal_load((it).src + (size_t)(2 * i_) * (it).stride); } while (0)
; __device__ __forceinline__ MoeItem moe_item(const float* wg, const float* wu, const float* wd, const float* win, const float* wout, const float* wpn, const float* wpd, unsigned char* ws, int r, int lane) {
;     ...
;     const int mat = r / MOE_IE, q = r % MOE_IE, e = mat / 3, which = mat % 3, kb = q / 64, nb = q % 64, n0 = nb * 32;
;     const float* src = (which == 0 ? wg : (which == 1 ? wu : wd)) + (size_t)e * DM * DFF + (size_t)(kb * 128 + (lane >> 5)) * DFF + n0 + (lane & 31);
;     unsigned char* dst;
;     if (which < 2) dst = ws + WS_WGUT + ((size_t)(e * 16 + (n0 >> 7)) * 256 + which * 128 + (n0 & 127)) * DM;
;     else dst = ws + WS_WDT + ((size_t)e * DM + n0) * DFF;
;     MoeItem it; it.stride = DFF; it.dpitch = DM; it.src = src; it.dst = dst + kb * 128 + (size_t)(lane >> 3) * DM + 16 * (lane & 7); return it;
;     ...
;             const int it1 = gw + (j + 1) * NGW, it2 = gw + (j + 2) * NGW;
;             ib = moe_item(wg, wu, wd, win, wout, wpn, wpd, F.ws, it1 <= last ? it1 : last, F.lane); MOE_LOAD(vb, ib);
.LBB0_81:
	s_mov_b32 s92, 0
	s_add_i32 s4, s72, s3
	s_min_i32 s70, s4, s7
	s_cmp_lt_i32 s70, 0x19000
	s_mov_b64 s[42:43], -1
	s_cbranch_scc0 .LBB0_102
	s_cmp_lt_i32 s70, 0x18c00
	s_cbranch_scc0 .LBB0_99
	s_cmp_lt_i32 s70, 0x18000
	s_cbranch_scc0 .LBB0_89
	s_mov_b32 s92, 1
	s_ashr_i32 s4, s70, 31
	s_lshr_b32 s4, s4, 22
	s_add_i32 s4, s70, s4
	s_ashr_i32 s43, s4, 10
	s_and_b32 s4, s4, 0xfc00
	s_sub_i32 s44, s70, s4
	s_mul_hi_i32 s4, s70, 0x2aaaaaab
	s_lshr_b32 s42, s4, 31
	s_ashr_i32 s4, s4, 9
	s_add_i32 s42, s4, s42
	s_mul_hi_i32 s4, s43, 0x55555556
	s_lshr_b32 s45, s4, 31
	s_add_i32 s4, s4, s45
	s_mul_i32 s4, s4, 3
	s_sub_i32 s4, s43, s4
	s_sext_i32_i16 s43, s44
	s_bfe_u32 s43, s43, 0x60019
	s_add_i32 s71, s44, s43
	s_and_b32 s43, s71, 0xffc0
	s_sub_i32 s43, s44, s43
	s_sext_i32_i16 s84, s43
	s_lshl_b32 s44, s84, 5
	s_ashr_i32 s43, s42, 31
	s_ashr_i32 s45, s44, 31
	s_cmp_gt_i32 s4, 1
	s_mov_b64 s[68:69], -1
	s_cbranch_scc0 .LBB0_86
	s_lshl_b64 s[46:47], s[42:43], 22
	s_lshl_b64 s[68:69], s[44:45], 11
	s_lshr_b32 s99, s68, 4
	s_and_b32 s99, s99, 0x7000
	s_and_b32 s68, s68, 0xfff80000
	s_or_b32 s68, s68, s99
	s_add_u32 s46, s73, s46
	s_addc_u32 s47, s74, s47
	s_add_u32 s46, s46, s68
	s_addc_u32 s47, s47, s69
	s_mov_b64 s[68:69], 0
.LBB0_86:
	s_andn2_b64 vcc, exec, s[68:69]
	s_cbranch_vccnz .LBB0_88
	s_lshl_b32 s46, s42, 4
	s_ashr_i32 s47, s84, 2
	s_add_i32 s46, s47, s46
	s_ashr_i32 s47, s46, 31
	s_lshl_b32 s68, s4, 7
	s_lshl_b64 s[46:47], s[46:47], 8
	s_ashr_i32 s69, s68, 31
	s_add_u32 s46, s46, s68
	s_addc_u32 s47, s47, s69
	s_and_b32 s68, s44, 0x60
	s_or_b32 s46, s46, s68
	s_lshl_b64 s[46:47], s[46:47], 11
	s_lshr_b32 s99, s46, 4
	s_and_b32 s99, s99, 0x7000
	s_and_b32 s46, s46, 0xfff80000
	s_or_b32 s46, s46, s99
	s_add_u32 s46, s75, s46
	s_addc_u32 s47, s76, s47
.LBB0_88:
	s_sext_i32_i16 s68, s71
	s_lshr_b32 s68, s68, 6
	s_cmp_eq_u32 s4, 1
	s_cselect_b32 s69, s20, s24
	s_cselect_b32 s71, s21, s25
	s_cmp_eq_u32 s4, 0
	s_cselect_b32 s4, s17, s71
	s_cselect_b32 s69, s16, s69
	s_lshl_b64 s[42:43], s[42:43], 24
	s_sext_i32_i16 s68, s68
	s_add_u32 s42, s69, s42
	s_addc_u32 s43, s4, s43
	s_lshl_b32 s4, s68, 7
	v_or_b32_e32 v12, s4, v20
	v_ashrrev_i32_e32 v13, 31, v12
	v_lshlrev_b64 v[12:13], 13, v[12:13]
	v_lshl_add_u64 v[12:13], s[42:43], 0, v[12:13]
	s_ashr_i32 s42, s4, 31
	v_lshl_add_u64 v[12:13], s[44:45], 2, v[12:13]
	s_lshl_b32 s98, s4, 8
	s_add_u32 s44, s46, s98
	v_lshlrev_b32_e32 v4, 2, v8
	s_addc_u32 s45, s47, s42
	v_lshl_add_u64 v[16:17], v[12:13], 0, v[4:5]
	s_mov_b64 s[42:43], 0
	v_mov_b64_e32 v[12:13], s[44:45]

; #define MOE_LOAD(v, it) do { _Pragma("unroll") for (int i_ = 0; i_ < 64; ++i_) v[i_] = __builtin_nontemporal_load((it).src + (size_t)(2 * i_) * (it).stride); } while (0)
;     ...
;             ib = moe_item(wg, wu, wd, win, wout, wpn, wpd, F.ws, it1 <= last ? it1 : last, F.lane); MOE_LOAD(vb, ib);
.LBB0_105:
	s_lshl_b64 s[46:47], s[46:47], 3
	global_load_dword v93, v[16:17], off nt
	v_lshl_add_u64 v[16:17], v[16:17], 0, s[46:47]
	v_lshl_add_u64 v[94:95], v[16:17], 0, s[46:47]
	v_lshl_add_u64 v[96:97], v[94:95], 0, s[46:47]
	v_lshl_add_u64 v[102:103], v[96:97], 0, s[46:47]
	v_lshl_add_u64 v[104:105], v[102:103], 0, s[46:47]
	v_lshl_add_u64 v[106:107], v[104:105], 0, s[46:47]
	v_lshl_add_u64 v[108:109], v[106:107], 0, s[46:47]
	v_lshl_add_u64 v[110:111], v[108:109], 0, s[46:47]
	global_load_dword v101, v[16:17], off nt
	global_load_dword v99, v[94:95], off nt
	global_load_dword v100, v[96:97], off nt
	s_nop 0
	global_load_dword v97, v[102:103], off nt
	global_load_dword v98, v[104:105], off nt
	global_load_dword v95, v[106:107], off nt
	global_load_dword v96, v[108:109], off nt
	global_load_dword v94, v[110:111], off nt
	v_lshl_add_u64 v[16:17], v[110:111], 0, s[46:47]
	s_waitcnt vmcnt(9)
	ds_write2st64_b32 v28, v87, v92 offset1:1
	v_lshl_add_u64 v[102:103], v[16:17], 0, s[46:47]
	global_load_dword v124, v[16:17], off nt
	global_load_dword v104, v[102:103], off nt
	v_lshl_add_u64 v[16:17], v[102:103], 0, s[46:47]
	global_load_dword v114, v[16:17], off nt
	v_lshl_add_u64 v[16:17], v[16:17], 0, s[46:47]
	global_load_dword v105, v[16:17], off nt
	v_lshl_add_u64 v[16:17], v[16:17], 0, s[46:47]
	global_load_dword v115, v[16:17], off nt
	v_lshl_add_u64 v[16:17], v[16:17], 0, s[46:47]
	global_load_dword v106, v[16:17], off nt
	v_lshl_add_u64 v[16:17], v[16:17], 0, s[46:47]
	global_load_dword v116, v[16:17], off nt
	v_lshl_add_u64 v[16:17], v[16:17], 0, s[46:47]
	global_load_dword v107, v[16:17], off nt
	v_lshl_add_u64 v[16:17], v[16:17], 0, s[46:47]
	global_load_dword v117, v[16:17], off nt
	v_lshl_add_u64 v[16:17], v[16:17], 0, s[46:47]
	global_load_dword v108, v[16:17], off nt
	v_lshl_add_u64 v[16:17], v[16:17], 0, s[46:47]
	global_load_dword v118, v[16:17], off nt
	v_lshl_add_u64 v[16:17], v[16:17], 0, s[46:47]
	global_load_dword v109, v[16:17], off nt
	v_lshl_add_u64 v[16:17], v[16:17], 0, s[46:47]
	global_load_dword v119, v[16:17], off nt
	v_lshl_add_u64 v[16:17], v[16:17], 0, s[46:47]
	global_load_dword v110, v[16:17], off nt
	v_lshl_add_u64 v[16:17], v[16:17], 0, s[46:47]
	global_load_dword v120, v[16:17], off nt
	v_lshl_add_u64 v[16:17], v[16:17], 0, s[46:47]
	global_load_dword v111, v[16:17], off nt
	v_lshl_add_u64 v[16:17], v[16:17], 0, s[46:47]
	global_load_dword v121, v[16:17], off nt
	v_lshl_add_u64 v[16:17], v[16:17], 0, s[46:47]
	global_load_dword v112, v[16:17], off nt
	v_lshl_add_u64 v[16:17], v[16:17], 0, s[46:47]
	global_load_dword v122, v[16:17], off nt
	v_lshl_add_u64 v[16:17], v[16:17], 0, s[46:47]
	global_load_dword v102, v[16:17], off nt
	v_lshl_add_u64 v[16:17], v[16:17], 0, s[46:47]
	global_load_dword v103, v[16:17], off nt
	v_lshl_add_u64 v[16:17], v[16:17], 0, s[46:47]
	global_load_dword v113, v[16:17], off nt
	v_lshl_add_u64 v[16:17], v[16:17], 0, s[46:47]
	global_load_dword v123, v[16:17], off nt
	v_lshl_add_u64 v[16:17], v[16:17], 0, s[46:47]
	global_load_dword v125, v[16:17], off nt
	v_lshl_add_u64 v[16:17], v[16:17], 0, s[46:47]
	global_load_dword v126, v[16:17], off nt
	v_lshl_add_u64 v[16:17], v[16:17], 0, s[46:47]
	global_load_dword v127, v[16:17], off nt
	v_lshl_add_u64 v[16:17], v[16:17], 0, s[46:47]
	global_load_dword v128, v[16:17], off nt
	v_lshl_add_u64 v[16:17], v[16:17], 0, s[46:47]
	global_load_dword v129, v[16:17], off nt
	v_lshl_add_u64 v[16:17], v[16:17], 0, s[46:47]
	global_load_dword v130, v[16:17], off nt
	v_lshl_add_u64 v[16:17], v[16:17], 0, s[46:47]
	global_load_dword v131, v[16:17], off nt
	v_lshl_add_u64 v[16:17], v[16:17], 0, s[46:47]
	global_load_dword v132, v[16:17], off nt
	v_lshl_add_u64 v[16:17], v[16:17], 0, s[46:47]
	global_load_dword v133, v[16:17], off nt
	v_lshl_add_u64 v[16:17], v[16:17], 0, s[46:47]
	global_load_dword v134, v[16:17], off nt
	v_lshl_add_u64 v[16:17], v[16:17], 0, s[46:47]
	global_load_dword v135, v[16:17], off nt
	v_lshl_add_u64 v[16:17], v[16:17], 0, s[46:47]
	global_load_dword v136, v[16:17], off nt
	v_lshl_add_u64 v[16:17], v[16:17], 0, s[46:47]
	global_load_dword v137, v[16:17], off nt
	v_lshl_add_u64 v[16:17], v[16:17], 0, s[46:47]
	global_load_dword v138, v[16:17], off nt
	v_lshl_add_u64 v[16:17], v[16:17], 0, s[46:47]
	global_load_dword v139, v[16:17], off nt
	v_lshl_add_u64 v[16:17], v[16:17], 0, s[46:47]
	global_load_dword v140, v[16:17], off nt
	v_lshl_add_u64 v[16:17], v[16:17], 0, s[46:47]
	global_load_dword v141, v[16:17], off nt
	v_lshl_add_u64 v[16:17], v[16:17], 0, s[46:47]
	global_load_dword v142, v[16:17], off nt
	v_lshl_add_u64 v[16:17], v[16:17], 0, s[46:47]
	global_load_dword v143, v[16:17], off nt
	v_lshl_add_u64 v[16:17], v[16:17], 0, s[46:47]
	global_load_dword v144, v[16:17], off nt
	v_lshl_add_u64 v[16:17], v[16:17], 0, s[46:47]
	global_load_dword v146, v[16:17], off nt
	v_lshl_add_u64 v[16:17], v[16:17], 0, s[46:47]
	global_load_dword v147, v[16:17], off nt
	v_lshl_add_u64 v[16:17], v[16:17], 0, s[46:47]
	global_load_dword v148, v[16:17], off nt
	v_lshl_add_u64 v[16:17], v[16:17], 0, s[46:47]
	global_load_dword v149, v[16:17], off nt
	v_lshl_add_u64 v[16:17], v[16:17], 0, s[46:47]
	global_load_dword v151, v[16:17], off nt
	v_lshl_add_u64 v[16:17], v[16:17], 0, s[46:47]
	global_load_dword v152, v[16:17], off nt
	v_lshl_add_u64 v[16:17], v[16:17], 0, s[46:47]
	global_load_dword v153, v[16:17], off nt
	v_lshl_add_u64 v[16:17], v[16:17], 0, s[46:47]
	global_load_dword v154, v[16:17], off nt
	v_lshl_add_u64 v[16:17], v[16:17], 0, s[46:47]
	global_load_dword v155, v[16:17], off nt
	v_lshl_add_u64 v[16:17], v[16:17], 0, s[46:47]
	global_load_dword v157, v[16:17], off nt
	v_lshl_add_u64 v[16:17], v[16:17], 0, s[46:47]
	global_load_dword v158, v[16:17], off nt
	v_lshl_add_u64 v[16:17], v[16:17], 0, s[46:47]
	ds_write2st64_b32 v28, v91, v90 offset0:2 offset1:3
	ds_write2st64_b32 v28, v89, v88 offset0:4 offset1:5
	ds_write2st64_b32 v28, v86, v85 offset0:6 offset1:7
	ds_write2st64_b32 v21, v83, v84 offset0:8 offset1:9
	ds_write2st64_b32 v21, v79, v80 offset0:10 offset1:11
	ds_write2st64_b32 v21, v75, v76 offset0:12 offset1:13
	ds_write2st64_b32 v21, v71, v72 offset0:14 offset1:15
	ds_write2st64_b32 v22, v65, v66 offset0:16 offset1:17
	ds_write2st64_b32 v22, v61, v62 offset0:18 offset1:19
	ds_write2st64_b32 v22, v57, v58 offset0:20 offset1:21
	ds_write2st64_b32 v22, v53, v54 offset0:22 offset1:23
	ds_write2st64_b32 v23, v45, v46 offset0:24 offset1:25
	ds_write2st64_b32 v23, v35, v36 offset0:26 offset1:27
	ds_write2st64_b32 v23, v33, v34 offset0:28 offset1:29
	ds_write2st64_b32 v23, v31, v32 offset0:30 offset1:31
	ds_write2st64_b32 v24, v29, v30 offset0:32 offset1:33
	ds_write2st64_b32 v24, v81, v82 offset0:34 offset1:35
	ds_write2st64_b32 v24, v77, v78 offset0:36 offset1:37
	ds_write2st64_b32 v24, v73, v74 offset0:38 offset1:39
	ds_write2st64_b32 v25, v69, v70 offset0:40 offset1:41
	ds_write2st64_b32 v25, v67, v68 offset0:42 offset1:43
	ds_write2st64_b32 v25, v63, v64 offset0:44 offset1:45
	ds_write2st64_b32 v25, v59, v60 offset0:46 offset1:47
	ds_write2st64_b32 v26, v55, v56 offset0:48 offset1:49
	ds_write2st64_b32 v26, v51, v52 offset0:50 offset1:51
	global_load_dword v159, v[16:17], off nt
	ds_write2st64_b32 v26, v38, v39 offset0:52 offset1:53
	ds_write2st64_b32 v26, v40, v42 offset0:54 offset1:55
	ds_write2st64_b32 v27, v37, v41 offset0:56 offset1:57
	ds_write2st64_b32 v27, v43, v44 offset0:58 offset1:59
	ds_write2st64_b32 v27, v47, v48 offset0:60 offset1:61
	ds_write2st64_b32 v27, v49, v50 offset0:62 offset1:63
	s_waitcnt lgkmcnt(0)
	ds_read2_b32 v[16:17], v1 offset1:32
	v_mov_b32_e32 v30, 0
	ds_read2_b32 v[32:33], v1 offset0:128 offset1:160
	v_mov_b32_e32 v31, 0
	v_add_u32_e32 v145, 0x400, v1
	s_waitcnt lgkmcnt(1)
	v_mul_f32_e32 v4, 0x42800000, v16
	v_mul_f32_e32 v15, 0x42800000, v17
	ds_read2_b32 v[16:17], v1 offset0:64 offset1:96
	v_cvt_pk_fp8_f32 v30, v4, v15
	ds_read2_b32 v[34:35], v145 offset0:128 offset1:160
	v_add_u32_e32 v150, 0x400, v9
	ds_read2_b32 v[38:39], v150 offset0:128 offset1:160
	s_waitcnt lgkmcnt(2)
	v_mul_f32_e32 v4, 0x42800000, v16
	v_mul_f32_e32 v15, 0x42800000, v17
	ds_read2_b32 v[16:17], v1 offset0:192 offset1:224
	v_cvt_pk_fp8_f32 v30, v4, v15 op_sel:[0,0,1]
	v_mul_f32_e32 v4, 0x42800000, v32
	v_mul_f32_e32 v15, 0x42800000, v33
	v_cvt_pk_fp8_f32 v31, v4, v15
	s_waitcnt lgkmcnt(0)
	v_mul_f32_e32 v4, 0x42800000, v16
	v_mul_f32_e32 v15, 0x42800000, v17
	ds_read2_b32 v[16:17], v145 offset0:64 offset1:96
	ds_read2_b32 v[32:33], v145 offset1:32
	v_cvt_pk_fp8_f32 v31, v4, v15 op_sel:[0,0,1]
	v_lshl_add_u64 v[10:11], v[10:11], 0, v[6:7]
	v_add_u32_e32 v156, 0x400, v18
	s_waitcnt lgkmcnt(1)
	v_mul_f32_e32 v29, 0x42800000, v16
	v_mul_f32_e32 v36, 0x42800000, v17
	ds_read2_b32 v[16:17], v145 offset0:192 offset1:224
	s_waitcnt lgkmcnt(1)
	v_mul_f32_e32 v4, 0x42800000, v32
	v_mul_f32_e32 v15, 0x42800000, v33
	v_mov_b32_e32 v32, 0
	v_cvt_pk_fp8_f32 v32, v4, v15
	v_mul_f32_e32 v4, 0x42800000, v34
	v_mul_f32_e32 v15, 0x42800000, v35
	v_mov_b32_e32 v33, 0
	ds_read2_b32 v[34:35], v9 offset1:32
	v_cvt_pk_fp8_f32 v33, v4, v15
	s_waitcnt lgkmcnt(1)
	v_mul_f32_e32 v4, 0x42800000, v16
	v_mul_f32_e32 v15, 0x42800000, v17
	ds_read2_b32 v[16:17], v9 offset0:64 offset1:96
	v_cvt_pk_fp8_f32 v32, v29, v36 op_sel:[0,0,1]
	ds_read2_b32 v[36:37], v9 offset0:128 offset1:160
	v_cvt_pk_fp8_f32 v33, v4, v15 op_sel:[0,0,1]
	s_waitcnt lgkmcnt(2)
	v_mul_f32_e32 v4, 0x42800000, v34
	v_mul_f32_e32 v15, 0x42800000, v35
	v_mov_b32_e32 v34, 0
	v_cvt_pk_fp8_f32 v34, v4, v15
	s_waitcnt lgkmcnt(1)
	v_mul_f32_e32 v4, 0x42800000, v16
	v_mul_f32_e32 v15, 0x42800000, v17
	ds_read2_b32 v[16:17], v9 offset0:192 offset1:224
	s_waitcnt lgkmcnt(1)
	v_mul_f32_e32 v29, 0x42800000, v36
	v_mul_f32_e32 v36, 0x42800000, v37
	v_mov_b32_e32 v35, 0
	v_cvt_pk_fp8_f32 v35, v29, v36
	ds_read2_b32 v[36:37], v150 offset1:32
	v_cvt_pk_fp8_f32 v34, v4, v15 op_sel:[0,0,1]
	s_waitcnt lgkmcnt(1)
	v_mul_f32_e32 v4, 0x42800000, v16
	v_mul_f32_e32 v15, 0x42800000, v17
	ds_read2_b32 v[16:17], v150 offset0:64 offset1:96
	v_cvt_pk_fp8_f32 v35, v4, v15 op_sel:[0,0,1]
	s_waitcnt lgkmcnt(1)
	v_mul_f32_e32 v4, 0x42800000, v36
	v_mul_f32_e32 v15, 0x42800000, v37
	v_mov_b32_e32 v36, 0
	v_cvt_pk_fp8_f32 v36, v4, v15
	s_waitcnt lgkmcnt(0)
	v_mul_f32_e32 v4, 0x42800000, v16
	v_mul_f32_e32 v15, 0x42800000, v17
	ds_read2_b32 v[16:17], v150 offset0:192 offset1:224
	v_cvt_pk_fp8_f32 v36, v4, v15 op_sel:[0,0,1]
	v_mul_f32_e32 v4, 0x42800000, v38
	v_mul_f32_e32 v15, 0x42800000, v39
	v_mov_b32_e32 v37, 0
	v_cvt_pk_fp8_f32 v37, v4, v15
	s_waitcnt lgkmcnt(0)
	v_mul_f32_e32 v4, 0x42800000, v16
	v_mul_f32_e32 v15, 0x42800000, v17
	ds_read2_b32 v[16:17], v18 offset1:32
	v_cvt_pk_fp8_f32 v37, v4, v15 op_sel:[0,0,1]
	global_store_dwordx4 v[10:11], v[30:33], off sc0 sc1 nt
	ds_read2_b32 v[32:33], v18 offset0:64 offset1:96
	s_lshl_b64 s[38:39], s[38:39], 3
	s_waitcnt lgkmcnt(1)
	v_mul_f32_e32 v4, 0x42800000, v16
	v_mul_f32_e32 v15, 0x42800000, v17
	ds_read2_b32 v[16:17], v18 offset0:128 offset1:160
	v_mov_b32_e32 v30, 0
	v_cvt_pk_fp8_f32 v30, v4, v15
	s_waitcnt lgkmcnt(1)
	v_mul_f32_e32 v4, 0x42800000, v32
	v_mov_b32_e32 v31, 0
	s_waitcnt lgkmcnt(0)
; __device__ __forceinline__ MoeItem moe_item(const float* wg, const float* wu, const float* wd, const float* win, const float* wout, const float* wpn, const float* wpd, unsigned char* ws, int r, int lane) {
;     ...
;     const int mat = r / MOE_IE, q = r % MOE_IE, e = mat / 3, which = mat % 3, kb = q / 64, nb = q % 64, n0 = nb * 32;
;     const float* src = (which == 0 ? wg : (which == 1 ? wu : wd)) + (size_t)e * DM * DFF + (size_t)(kb * 128 + (lane >> 5)) * DFF + n0 + (lane & 31);
;     unsigned char* dst;
;     if (which < 2) dst = ws + WS_WGUT + ((size_t)(e * 16 + (n0 >> 7)) * 256 + which * 128 + (n0 & 127)) * DM;
;     else dst = ws + WS_WDT + ((size_t)e * DM + n0) * DFF;
;     MoeItem it; it.stride = DFF; it.dpitch = DM; it.src = src; it.dst = dst + kb * 128 + (size_t)(lane >> 3) * DM + 16 * (lane & 7); return it;
	v_mul_f32_e32 v29, 0x42800000, v16
	v_mul_f32_e32 v32, 0x42800000, v17
	ds_read2_b32 v[16:17], v18 offset0:192 offset1:224
	v_mul_f32_e32 v15, 0x42800000, v33
	v_cvt_pk_fp8_f32 v31, v29, v32
	ds_read2_b32 v[32:33], v156 offset1:32
	v_cvt_pk_fp8_f32 v30, v4, v15 op_sel:[0,0,1]
	s_waitcnt lgkmcnt(1)
	v_mul_f32_e32 v4, 0x42800000, v16
	v_mul_f32_e32 v15, 0x42800000, v17
	ds_read2_b32 v[16:17], v156 offset0:64 offset1:96
	v_lshl_add_u64 v[10:11], v[10:11], 0, s[38:39]
	global_store_dwordx4 v[10:11], v[34:37], off sc0 sc1 nt
	ds_read2_b32 v[34:35], v156 offset0:128 offset1:160
	v_cvt_pk_fp8_f32 v31, v4, v15 op_sel:[0,0,1]
	s_waitcnt lgkmcnt(2)
	v_mul_f32_e32 v4, 0x42800000, v32
	v_mul_f32_e32 v15, 0x42800000, v33
	v_mov_b32_e32 v32, 0
	v_cvt_pk_fp8_f32 v32, v4, v15
	s_waitcnt lgkmcnt(1)
	v_mul_f32_e32 v4, 0x42800000, v16
	v_mul_f32_e32 v15, 0x42800000, v17
	ds_read2_b32 v[16:17], v156 offset0:192 offset1:224
	s_waitcnt lgkmcnt(1)
	v_mul_f32_e32 v29, 0x42800000, v34
	v_mul_f32_e32 v34, 0x42800000, v35
	v_mov_b32_e32 v33, 0
	v_cvt_pk_fp8_f32 v33, v29, v34
	ds_read2_b32 v[34:35], v19 offset1:32
	v_cvt_pk_fp8_f32 v32, v4, v15 op_sel:[0,0,1]
	s_waitcnt lgkmcnt(1)
	v_mul_f32_e32 v4, 0x42800000, v16
	v_mul_f32_e32 v15, 0x42800000, v17
	ds_read2_b32 v[16:17], v19 offset0:64 offset1:96
	ds_read2_b32 v[36:37], v19 offset0:128 offset1:160
	v_cvt_pk_fp8_f32 v33, v4, v15 op_sel:[0,0,1]
	s_waitcnt lgkmcnt(2)
	v_mul_f32_e32 v4, 0x42800000, v34
	v_mul_f32_e32 v15, 0x42800000, v35
	v_mov_b32_e32 v34, 0
	v_cvt_pk_fp8_f32 v34, v4, v15
	s_waitcnt lgkmcnt(1)
	v_mul_f32_e32 v4, 0x42800000, v16
	v_mul_f32_e32 v15, 0x42800000, v17
	ds_read2_b32 v[16:17], v19 offset0:192 offset1:224
	s_waitcnt lgkmcnt(1)
	v_mul_f32_e32 v29, 0x42800000, v36
	v_mul_f32_e32 v36, 0x42800000, v37
	v_mov_b32_e32 v35, 0
	v_add_u32_e32 v160, 0x400, v19
	v_cvt_pk_fp8_f32 v35, v29, v36
	ds_read2_b32 v[36:37], v160 offset1:32
	v_cvt_pk_fp8_f32 v34, v4, v15 op_sel:[0,0,1]
	s_waitcnt lgkmcnt(1)
	v_mul_f32_e32 v4, 0x42800000, v16
	v_mul_f32_e32 v15, 0x42800000, v17
	ds_read2_b32 v[16:17], v160 offset0:64 offset1:96
	ds_read2_b32 v[38:39], v160 offset0:128 offset1:160
	v_cvt_pk_fp8_f32 v35, v4, v15 op_sel:[0,0,1]
	s_waitcnt lgkmcnt(2)
	v_mul_f32_e32 v4, 0x42800000, v36
	v_mul_f32_e32 v15, 0x42800000, v37
	v_mov_b32_e32 v36, 0
	v_cvt_pk_fp8_f32 v36, v4, v15
	s_waitcnt lgkmcnt(1)
	v_mul_f32_e32 v4, 0x42800000, v16
	v_mul_f32_e32 v15, 0x42800000, v17
	ds_read2_b32 v[16:17], v160 offset0:192 offset1:224
	s_waitcnt lgkmcnt(1)
	v_mul_f32_e32 v29, 0x42800000, v38
	v_mul_f32_e32 v38, 0x42800000, v39
	v_mov_b32_e32 v37, 0
	v_cvt_pk_fp8_f32 v37, v29, v38
	v_cvt_pk_fp8_f32 v36, v4, v15 op_sel:[0,0,1]
	s_waitcnt lgkmcnt(0)
	v_mul_f32_e32 v4, 0x42800000, v16
	v_mul_f32_e32 v15, 0x42800000, v17
	v_cvt_pk_fp8_f32 v37, v4, v15 op_sel:[0,0,1]
	v_lshl_add_u64 v[10:11], v[10:11], 0, s[38:39]
	global_store_dwordx4 v[10:11], v[30:33], off sc0 sc1 nt
	v_lshl_add_u64 v[10:11], v[10:11], 0, s[38:39]
	global_store_dwordx4 v[10:11], v[34:37], off sc0 sc1 nt
	s_waitcnt lgkmcnt(0)
	s_add_i32 s3, s89, s3
	s_mov_b32 s96, 0
	s_min_i32 s43, s3, s7
	s_cmp_lt_i32 s43, 0x19000
	s_mov_b64 s[38:39], -1
	s_cbranch_scc0 .LBB0_126
	s_cmp_lt_i32 s43, 0x18c00
	s_cbranch_scc0 .LBB0_123
	s_cmp_lt_i32 s43, 0x18000
	s_cbranch_scc0 .LBB0_113
	s_mov_b32 s96, 1
	s_ashr_i32 s4, s43, 31
	s_lshr_b32 s4, s4, 22
	s_add_i32 s4, s43, s4
	s_ashr_i32 s39, s4, 10
	s_and_b32 s4, s4, 0xfc00
	s_sub_i32 s46, s43, s4
	s_mul_hi_i32 s4, s43, 0x2aaaaaab
	s_lshr_b32 s38, s4, 31
	s_ashr_i32 s4, s4, 9
	s_add_i32 s38, s4, s38
	s_mul_hi_i32 s4, s39, 0x55555556
	s_lshr_b32 s45, s4, 31
	s_add_i32 s4, s4, s45
	s_mul_i32 s4, s4, 3
	s_sub_i32 s4, s39, s4
	s_sext_i32_i16 s39, s46
	s_bfe_u32 s39, s39, 0x60019
	s_add_i32 s45, s46, s39
	s_and_b32 s39, s45, 0xffc0
	s_sub_i32 s39, s46, s39
	s_sext_i32_i16 s84, s39
	s_lshl_b32 s46, s84, 5
	s_ashr_i32 s39, s38, 31
	s_ashr_i32 s47, s46, 31
	s_cmp_gt_i32 s4, 1
	s_mov_b64 s[70:71], -1
	s_cbranch_scc0 .LBB0_110
	s_lshl_b64 s[68:69], s[38:39], 22
	s_lshl_b64 s[70:71], s[46:47], 11
	s_lshr_b32 s99, s70, 4
	s_and_b32 s99, s99, 0x7000
	s_and_b32 s70, s70, 0xfff80000
	s_or_b32 s70, s70, s99
	s_add_u32 s68, s73, s68
	s_addc_u32 s69, s74, s69
	s_add_u32 s68, s68, s70
	s_addc_u32 s69, s69, s71
	s_mov_b64 s[70:71], 0
.LBB0_110:
	s_andn2_b64 vcc, exec, s[70:71]
	s_cbranch_vccnz .LBB0_112
	s_lshl_b32 s68, s38, 4
	s_ashr_i32 s69, s84, 2
	s_add_i32 s68, s69, s68
	s_ashr_i32 s69, s68, 31
	s_lshl_b32 s70, s4, 7
	s_lshl_b64 s[68:69], s[68:69], 8
	s_ashr_i32 s71, s70, 31
	s_add_u32 s68, s68, s70
	s_addc_u32 s69, s69, s71
	s_and_b32 s70, s46, 0x60
	s_or_b32 s68, s68, s70
	s_lshl_b64 s[68:69], s[68:69], 11
	s_lshr_b32 s99, s68, 4
	s_and_b32 s99, s99, 0x7000
	s_and_b32 s68, s68, 0xfff80000
	s_or_b32 s68, s68, s99
	s_add_u32 s68, s75, s68
	s_addc_u32 s69, s76, s69
.LBB0_112:
	s_sext_i32_i16 s45, s45
	s_lshr_b32 s45, s45, 6
	s_cmp_eq_u32 s4, 1
	s_cselect_b32 s70, s20, s24
	s_cselect_b32 s71, s21, s25
	s_cmp_eq_u32 s4, 0
	s_cselect_b32 s4, s17, s71
	s_cselect_b32 s70, s16, s70
	s_lshl_b64 s[38:39], s[38:39], 24
	s_sext_i32_i16 s45, s45
	s_add_u32 s38, s70, s38
	s_addc_u32 s39, s4, s39
	s_lshl_b32 s4, s45, 7
	v_or_b32_e32 v10, s4, v20
	v_ashrrev_i32_e32 v11, 31, v10
	v_lshlrev_b64 v[10:11], 13, v[10:11]
	v_lshl_add_u64 v[10:11], s[38:39], 0, v[10:11]
	s_ashr_i32 s38, s4, 31
	v_lshl_add_u64 v[10:11], s[46:47], 2, v[10:11]
	s_lshl_b32 s98, s4, 8
	s_add_u32 s46, s68, s98
	v_mov_b32_e32 v15, v5
	s_addc_u32 s47, s69, s38
	v_lshl_add_u64 v[16:17], v[10:11], 0, v[14:15]
	s_mov_b64 s[38:39], 0
	v_mov_b64_e32 v[10:11], s[46:47]

; #define PG8_STAGE(bufoff, gbase, voff) do { _Pragma("unroll") for (int _i = 0; _i < 2; ++_i) \
;         __builtin_amdgcn_global_load_lds((const unsigned*)((const char*)(gbase) + (voff)[_i]), (LAS unsigned*)(lds + (bufoff) + ldsw + _i * 8192), 16, 0, 0); } while (0)
; #define PG8_WAIT_V(n) asm volatile("s_waitcnt vmcnt(" #n ")" ::: "memory")
; #define PG8_BAR __builtin_amdgcn_s_barrier()
; template <class Epi, class Sched, bool GATHER, bool F8 = false>
; __device__ __forceinline__ void gemm_phase(LAS unsigned char* lds, const int K, const Sched& S, const Epi& E) {
;     ...
;     if constexpr (EpiInit<Epi>::value) { const typename EpiInit<Epi>::Pre p0 = E.preload(cur, wr, wc, fr, fq); E.init(acc, p0); }
;     int one_scale = 0x7f7f7f7f; asm volatile("" : "+v"(one_scale));
;     bf16x8 At[4][2], B0[2][2], B1[2][2]; i32x8 At8[4], B08[2], B18[2];
;     const char* cA = cur.A; const char* cB = cur.B;
;     PG8_STAGE(PG8_SB(0, 0), cB, voffB); PG8_STAGE(PG8_SB(0, 1), cB + hstepB, voffB); PG8_STAGE(PG8_SA(0, 0), cA, vA[0]); PG8_STAGE(PG8_SA(0, 1), cA, vA[1]);
;     if (wr == 1) PG8_BAR;
;     PG8_WAIT_V(2); PG8_BAR;
;     PG8_STAGE(PG8_SB(1, 0), cB + kstep, voffB); PG8_STAGE(PG8_SA(1, 0), cA + kstep, vA[0]); PG8_STAGE(PG8_SB(1, 1), cB + hstepB + kstep, voffB);
;     PG8_WAIT_V(6); PG8_BAR;
.LBB0_1027:
	s_or_b64 exec, exec, s[10:11]
	v_and_b32_e32 v2, 0x100, v0
	v_mov_b32_e32 v5, 2
	s_add_i32 s0, 0, 0x20000
	v_lshlrev_b32_e32 v2, 2, v2
	v_lshlrev_b32_sdwa v5, v5, v0 dst_sel:DWORD dst_unused:UNUSED_PAD src0_sel:DWORD src1_sel:BYTE_0
	s_or_b32 s6, s6, s7
	v_add3_u32 v2, s0, v2, v5
	s_cmp_ge_i32 s6, s3
	v_readfirstlane_b32 s20, v0
	s_waitcnt vmcnt(0)
	ds_write2st64_b32 v2, v4, v1 offset0:8 offset1:16
	ds_write2st64_b32 v2, v7, v6 offset0:24 offset1:32
	ds_write_b32 v2, v3 offset:10240
	s_waitcnt lgkmcnt(0)
	s_barrier
	s_cbranch_scc1 .LBB0_1045
	v_lshlrev_b32_e32 v1, 4, v0
	v_and_b32_e32 v2, 32, v0
	v_bfe_u32 v4, v0, 3, 25
	s_add_u32 s7, s82, 0x4000000
	v_bfe_u32 v3, v0, 2, 4
	v_bitop3_b32 v1, v1, v2, 48 bitop3:0x6c
	v_lshrrev_b32_e32 v2, 3, v0
	v_or_b32_e32 v4, 64, v4
	s_movk_i32 s0, 0x70
	s_addc_u32 s25, s83, 0
	v_and_or_b32 v160, v2, 48, v3
	v_and_or_b32 v161, v4, s0, v3
	s_lshl_b32 s0, s20, 4
	v_lshrrev_b32_e32 v3, 1, v0
	s_and_b32 s37, s0, 0xfffffc00
	v_and_b32_e32 v14, 24, v3
	s_lshr_b32 s0, s20, 1
	v_lshrrev_b32_e32 v3, 5, v0
	s_lshr_b32 s21, s20, 8
	s_and_b32 s14, s0, 0x60
	v_and_b32_e32 v3, 4, v3
	v_bfe_u32 v5, v0, 2, 2
	s_movk_i32 s10, 0x60
	s_add_u32 s0, s82, 0x2c000000
	v_or3_b32 v3, v3, v5, v14
	s_addc_u32 s1, s83, 0
	v_and_or_b32 v4, v4, s10, v3
	s_lshl_b32 s10, s6, 2
	s_add_i32 s10, s10, 0
	v_and_or_b32 v1, v0, 64, v1
	v_and_or_b32 v2, v2, 32, v3
	s_add_i32 s10, s10, 0x20000
	v_lshl_or_b32 v148, v2, 11, v1
	v_mov_b32_e32 v2, s10
	ds_read_b32 v150, v2
	s_lshl_b32 s10, s2, 3
	s_and_b32 s39, s10, 8
	s_ashr_i32 s10, s2, 5
	s_add_i32 s39, s39, s10
	s_waitcnt lgkmcnt(0)
	v_readfirstlane_b32 s10, v150
	s_lshl_b32 s10, s10, 4
	s_add_i32 s10, s10, s39
	s_ashr_i32 s11, s10, 31
	s_lshl_b64 s[10:11], s[10:11], 19
	s_add_u32 s44, s7, s10
	v_lshl_or_b32 v146, v4, 11, v1
	v_lshrrev_b32_e32 v254, 11, v148
	v_and_b32_e32 v148, 0x7f, v148
	v_lshl_or_b32 v148, v254, 7, v148
	v_lshrrev_b32_e32 v254, 11, v146
	v_and_b32_e32 v146, 0x7f, v146
	v_lshl_or_b32 v146, v254, 7, v146
	s_addc_u32 s45, s25, s11
	s_add_i32 s10, 0, 0x20800
	v_lshlrev_b32_e32 v2, 2, v160
	v_lshlrev_b32_e32 v4, 2, v161
	v_add_u32_e32 v3, s10, v2
	v_add_u32_e32 v5, s10, v4
	s_add_i32 s10, 0, 0x20a00
	v_add_u32_e32 v2, s10, v2
	v_add_u32_e32 v4, s10, v4
	ds_read_b32 v3, v3
	ds_read_b32 v5, v5
	ds_read_b32 v2, v2
	ds_read_b32 v4, v4
	s_lshl_b32 s50, s39, 7
	v_or_b32_e32 v162, s14, v14
	v_ashrrev_i32_e32 v151, 31, v150
	s_waitcnt lgkmcnt(1)
	v_lshl_or_b32 v163, v2, 11, v1
	v_or_b32_e32 v2, s50, v162
	v_lshl_or_b32 v152, v3, 11, v1
	v_lshl_or_b32 v154, v5, 11, v1
	s_waitcnt lgkmcnt(0)
	v_lshl_or_b32 v164, v4, 11, v1
	v_lshlrev_b64 v[4:5], 13, v[150:151]
	v_ashrrev_i32_e32 v3, 31, v2
	v_lshl_add_u64 v[6:7], s[18:19], 0, v[4:5]
	v_lshlrev_b64 v[2:3], 2, v[2:3]
	s_add_i32 s51, s37, 0
	v_lshl_add_u64 v[10:11], v[6:7], 0, v[2:3]
	v_lshl_add_u64 v[4:5], s[22:23], 0, v[4:5]
	v_mov_b32_e32 v165, 0x7f7f7f7f
	s_add_i32 m0, s51, 0x10000
	v_lshl_add_u64 v[12:13], v[4:5], 0, v[2:3]
	global_load_dwordx4 v[58:61], v[10:11], off offset:16
	global_load_dwordx4 v[62:65], v[10:11], off
	global_load_dwordx4 v[2:5], v[12:13], off offset:16
	global_load_dwordx4 v[6:9], v[12:13], off
	global_load_lds_dwordx4 v148, s[44:45]
	s_add_i32 m0, s51, 0x12000
	s_add_u32 s10, s44, 0x4000
	global_load_lds_dwordx4 v146, s[44:45]
	s_addc_u32 s11, s45, 0
	s_add_i32 m0, s51, 0x14000
	s_add_i32 s52, s51, 0x2000
	global_load_lds_dwordx4 v148, s[10:11]
	s_add_i32 m0, s51, 0x16000
	s_add_i32 s53, s51, 0x4000
	global_load_lds_dwordx4 v146, s[10:11]
	s_mov_b32 m0, s51
	s_add_i32 s54, s51, 0x6000
	global_load_lds_dwordx4 v152, s[0:1]
	s_mov_b32 m0, s52
	v_mov_b32_e32 v153, 0
	global_load_lds_dwordx4 v154, s[0:1]
	s_mov_b32 m0, s53
	v_mov_b32_e32 v149, v153
	global_load_lds_dwordx4 v163, s[0:1]
	s_mov_b32 m0, s54
	v_mov_b32_e32 v147, v153
	global_load_lds_dwordx4 v164, s[0:1]
	s_cmp_eq_u32 s21, 1
	v_lshl_add_u64 v[12:13], s[44:45], 0, v[148:149]
	v_lshl_add_u64 v[10:11], s[44:45], 0, v[146:147]
	s_cselect_b64 s[10:11], -1, 0
	s_cmp_lg_u32 s21, 1
	v_mov_b32_e32 v155, v153
	s_cbranch_scc1 .LBB0_1030
	s_barrier
.LBB0_1030:
	s_lshl_b32 s64, s6, 8
	s_add_u32 s12, s82, 0x34000000
	s_addc_u32 s13, s83, 0
	s_lshl_b32 s36, s14, 7
	s_mov_b64 s[14:15], 0x80
	s_mov_b64 s[100:101], 0x8000
	s_add_i32 m0, s51, 0x18000
	v_lshl_add_u64 v[12:13], v[12:13], 0, s[100:101]
	s_lshl_b32 s24, s21, 13
	s_waitcnt vmcnt(2)
	s_barrier
	global_load_lds_dwordx4 v[12:13], off
	s_add_i32 m0, s51, 0x1a000
	s_add_u32 s16, s82, 0x2c000080
	v_lshl_add_u64 v[10:11], v[10:11], 0, s[100:101]
	s_addc_u32 s17, s83, 0
	s_add_i32 s55, s51, 0x8000
	s_add_i32 s56, s51, 0xa000
	global_load_lds_dwordx4 v[10:11], off
	v_lshl_add_u64 v[10:11], s[16:17], 0, v[152:153]
	s_mov_b32 m0, s55
	s_add_u32 s40, s44, 0xc000
	global_load_lds_dwordx4 v[10:11], off
	v_lshl_add_u64 v[10:11], s[16:17], 0, v[154:155]
	s_mov_b32 m0, s56
	s_addc_u32 s41, s45, 0
	global_load_lds_dwordx4 v[10:11], off
	s_add_i32 m0, s51, 0x1c000
	v_lshl_add_u64 v[10:11], s[40:41], 0, v[148:149]
	global_load_lds_dwordx4 v[10:11], off
	v_lshl_add_u64 v[10:11], s[40:41], 0, v[146:147]
	s_add_i32 m0, s51, 0x1e000
	v_lshlrev_b32_e32 v12, 2, v0
	global_load_lds_dwordx4 v[10:11], off
	v_and_b32_e32 v10, 15, v0
	v_lshlrev_b32_e32 v11, 1, v14
	v_lshl_or_b32 v166, s21, 6, v10
	v_lshl_or_b32 v10, v10, 6, v11
	v_and_b32_e32 v12, 32, v12
	v_lshlrev_b32_e32 v13, 6, v0
	s_movk_i32 s21, 0x3c0
	s_waitcnt vmcnt(6)
	v_bitop3_b32 v10, v10, s24, v12 bitop3:0xde
	v_and_or_b32 v11, v13, s21, v11
	s_cmpk_lt_u32 s20, 0x100
	v_bitop3_b32 v167, s36, v11, v12 bitop3:0xf6
	s_mov_b32 s57, 0
	s_cselect_b64 s[20:21], -1, 0
	s_mov_b32 s24, 0x42800000
	s_add_i32 s58, 0, 0x10000
	s_add_i32 s59, 0, 0x14000
	v_add_u32_e32 v168, 0, v10
	s_mov_b32 s36, 0x3c800000
	s_mov_b32 s60, 0xc0c00000
	s_mov_b32 s38, 0xc01d265f
	s_add_i32 s61, s51, 0xc000
	s_add_i32 s62, s51, 0xe000
	v_mov_b32_e32 v169, 0x41000000
	s_mov_b64 s[40:41], s[44:45]
	s_barrier
	s_branch .LBB0_1033

; #define PG8_STAGE(bufoff, gbase, voff) do { _Pragma("unroll") for (int _i = 0; _i < 2; ++_i) \
;         __builtin_amdgcn_global_load_lds((const unsigned*)((const char*)(gbase) + (voff)[_i]), (LAS unsigned*)(lds + (bufoff) + ldsw + _i * 8192), 16, 0, 0); } while (0)
; #define PG8_LDA(dst, b, h) do { _Pragma("unroll") for (int m = 0; m < 4; ++m) { if constexpr (F8) dst##8[m] = PG8_LD32(lds + PG8_SA(b, h) + aoff + m * 2048); \
;         else { _Pragma("unroll") for (int k = 0; k < 2; ++k) dst[m][k] = *(const LAS bf16x8*)(lds + PG8_SA(b, h) + aoff + m * 2048 + k * 1024); } } } while (0)
; #define PG8_LDB(dst, b, h) do { _Pragma("unroll") for (int n = 0; n < 2; ++n) { if constexpr (F8) dst##8[n] = PG8_LD32(lds + PG8_SB(b, h) + boff + n * 2048); \
;         else { _Pragma("unroll") for (int k = 0; k < 2; ++k) dst[n][k] = *(const LAS bf16x8*)(lds + PG8_SB(b, h) + boff + n * 2048 + k * 1024); } } } while (0)
; #define PG8_WAIT_V(n) asm volatile("s_waitcnt vmcnt(" #n ")" ::: "memory")
; #define PG8_WAIT_L(n) asm volatile("s_waitcnt lgkmcnt(" #n ")" ::: "memory")
; #define PG8_BAR __builtin_amdgcn_s_barrier()
; #define PG8_SCHED __builtin_amdgcn_sched_barrier(0)
; template <class Epi, class Sched, bool GATHER, bool F8 = false>
; __device__ __forceinline__ void gemm_phase(LAS unsigned char* lds, const int K, const Sched& S, const Epi& E) {
;     ...
;             PG8_LDB(B0, 0, 0); PG8_LDB(B1, 0, 1); PG8_SCHED; PG8_LDA(At, 0, 0); PG8_STAGE(PG8_SA(1, 1), a1, vA[1]);
;             PG8_WAIT_V(8); PG8_WAIT_L(0); PG8_BAR; PG8_MMA(0, 0, At, B0); PG8_MMA(0, 1, At, B1); PG8_BAR; PG8_SCHED;
;     __device__ __forceinline__ void init(f32x4 (&acc)[2][2][4][2], const Pre& p) const {
; #pragma unroll
;         for (int ai = 0; ai < 2; ++ai)
; #pragma unroll
;             for (int m = 0; m < 4; ++m)
; #pragma unroll
;                 for (int n = 0; n < 2; ++n) { acc[ai][0][m][n] = p.g[n] * WSCALE; acc[ai][1][m][n] = (p.u[n] + 1.0f) * WSCALE; }
;     }
.LBB0_1035:
	s_lshl_b32 s46, s57, 10
	s_waitcnt vmcnt(0)
	v_pk_add_f32 v[8:9], v[8:9], 1.0 op_sel_hi:[1,0]
	v_pk_add_f32 v[4:5], v[4:5], 1.0 op_sel_hi:[1,0]
	s_add_i32 s46, s46, 0
	v_pk_mul_f32 v[20:21], v[64:65], s[24:25] op_sel_hi:[1,0]
	v_pk_mul_f32 v[12:13], v[60:61], s[24:25] op_sel_hi:[1,0]
	v_pk_add_f32 v[6:7], v[6:7], 1.0 op_sel_hi:[1,0]
	v_pk_mul_f32 v[24:25], v[8:9], s[24:25] op_sel_hi:[1,0]
	v_pk_add_f32 v[2:3], v[2:3], 1.0 op_sel_hi:[1,0]
	v_pk_mul_f32 v[16:17], v[4:5], s[24:25] op_sel_hi:[1,0]
	s_add_i32 s46, s46, 0x20800
	v_pk_mul_f32 v[18:19], v[62:63], s[24:25] op_sel_hi:[1,0]
	v_pk_mul_f32 v[10:11], v[58:59], s[24:25] op_sel_hi:[1,0]
	v_pk_mul_f32 v[22:23], v[6:7], s[24:25] op_sel_hi:[1,0]
	v_pk_mul_f32 v[14:15], v[2:3], s[24:25] op_sel_hi:[1,0]
	s_add_u32 s65, s44, 0x10000
	v_mov_b64_e32 v[28:29], v[16:17]
	v_mov_b64_e32 v[36:37], v[24:25]
	v_mov_b64_e32 v[44:45], v[16:17]
	v_mov_b64_e32 v[52:53], v[24:25]
	v_mov_b64_e32 v[68:69], v[16:17]
	v_mov_b64_e32 v[76:77], v[24:25]
	v_mov_b64_e32 v[32:33], v[12:13]
	v_mov_b64_e32 v[40:41], v[20:21]
	v_mov_b64_e32 v[48:49], v[12:13]
	v_mov_b64_e32 v[56:57], v[20:21]
	v_mov_b64_e32 v[72:73], v[12:13]
	v_mov_b64_e32 v[80:81], v[20:21]
	v_mov_b64_e32 v[84:85], v[16:17]
	v_mov_b64_e32 v[92:93], v[24:25]
	v_mov_b64_e32 v[100:101], v[16:17]
	v_mov_b64_e32 v[108:109], v[24:25]
	v_mov_b64_e32 v[116:117], v[16:17]
	v_mov_b64_e32 v[124:125], v[24:25]
	v_mov_b64_e32 v[132:133], v[16:17]
	v_mov_b64_e32 v[140:141], v[24:25]
	v_mov_b64_e32 v[88:89], v[12:13]
	v_mov_b64_e32 v[96:97], v[20:21]
	v_mov_b64_e32 v[104:105], v[12:13]
	v_mov_b64_e32 v[112:113], v[20:21]
	v_mov_b64_e32 v[120:121], v[12:13]
	v_mov_b64_e32 v[128:129], v[20:21]
	v_mov_b64_e32 v[136:137], v[12:13]
	v_mov_b64_e32 v[144:145], v[20:21]
	v_mov_b32_e32 v58, v163
	v_mov_b32_e32 v59, v153
	v_mov_b32_e32 v60, v164
	v_mov_b32_e32 v61, v153
	v_lshl_add_u32 v151, v160, 2, s46
	v_lshl_add_u32 v171, v161, 2, s46
	s_addc_u32 s66, s45, 0
	s_mov_b32 s67, -2
	s_mov_b64 s[44:45], s[16:17]
	v_mov_b64_e32 v[26:27], v[14:15]
	v_mov_b64_e32 v[34:35], v[22:23]
	v_mov_b64_e32 v[42:43], v[14:15]
	v_mov_b64_e32 v[50:51], v[22:23]
	v_mov_b64_e32 v[66:67], v[14:15]
	v_mov_b64_e32 v[74:75], v[22:23]
	v_mov_b64_e32 v[30:31], v[10:11]
	v_mov_b64_e32 v[38:39], v[18:19]
	v_mov_b64_e32 v[46:47], v[10:11]
	v_mov_b64_e32 v[54:55], v[18:19]
	v_mov_b64_e32 v[70:71], v[10:11]
	v_mov_b64_e32 v[78:79], v[18:19]
	v_mov_b64_e32 v[82:83], v[14:15]
	v_mov_b64_e32 v[90:91], v[22:23]
	v_mov_b64_e32 v[98:99], v[14:15]
	v_mov_b64_e32 v[106:107], v[22:23]
	v_mov_b64_e32 v[114:115], v[14:15]
	v_mov_b64_e32 v[122:123], v[22:23]
	v_mov_b64_e32 v[130:131], v[14:15]
	v_mov_b64_e32 v[138:139], v[22:23]
	v_mov_b64_e32 v[86:87], v[10:11]
	v_mov_b64_e32 v[94:95], v[18:19]
	v_mov_b64_e32 v[102:103], v[10:11]
	v_mov_b64_e32 v[110:111], v[18:19]
	v_mov_b64_e32 v[118:119], v[10:11]
	v_mov_b64_e32 v[126:127], v[18:19]
	v_mov_b64_e32 v[134:135], v[10:11]
	v_mov_b64_e32 v[142:143], v[18:19]
	s_branch .LBB0_1037
.LBB0_1036:
	v_add_u32_e32 v62, s58, v167
	ds_read_b128 v[2:5], v62
	ds_read_b128 v[6:9], v62 offset:1024
	ds_read_b128 v[172:175], v62 offset:2048
	ds_read_b128 v[176:179], v62 offset:3072
	v_add_u32_e32 v62, s59, v167
	ds_read_b128 v[180:183], v62
	ds_read_b128 v[184:187], v62 offset:1024
	ds_read_b128 v[188:191], v62 offset:2048
	ds_read_b128 v[192:195], v62 offset:3072
	s_add_u32 s48, s44, 0x80
	s_addc_u32 s49, s45, 0
	s_and_b64 s[46:47], s[46:47], exec
	s_cselect_b32 s49, s1, s49
	s_cselect_b32 s48, s0, s48
	s_cselect_b32 s47, s41, s66
	s_cselect_b32 s46, s40, s65
	s_mov_b32 m0, s61
	v_lshl_add_u64 v[62:63], s[44:45], 0, v[58:59]
	ds_read_b128 v[196:199], v168
	ds_read_b128 v[200:203], v168 offset:1024
	ds_read_b128 v[204:207], v168 offset:2048
	ds_read_b128 v[208:211], v168 offset:3072
	ds_read_b128 v[212:215], v168 offset:4096
	ds_read_b128 v[216:219], v168 offset:5120
	ds_read_b128 v[220:223], v168 offset:6144
	ds_read_b128 v[224:227], v168 offset:7168
	global_load_lds_dwordx4 v[62:63], off
	v_lshl_add_u64 v[62:63], s[44:45], 0, v[60:61]
	s_mov_b32 m0, s62
	s_nop 0
	global_load_lds_dwordx4 v[62:63], off
	s_waitcnt vmcnt(8)
	s_waitcnt lgkmcnt(0)
	s_barrier
	s_setprio 1
	s_waitcnt lgkmcnt(0)
	v_mfma_scale_f32_16x16x128_f8f6f4 v[142:145], v[2:9], v[196:203], v[142:145], v165, v165 op_sel_hi:[0,0,0]
	v_mfma_scale_f32_16x16x128_f8f6f4 v[134:137], v[172:179], v[196:203], v[134:137], v165, v165 op_sel_hi:[0,0,0]
	v_mfma_scale_f32_16x16x128_f8f6f4 v[126:129], v[2:9], v[204:211], v[126:129], v165, v165 op_sel_hi:[0,0,0]
	v_mfma_scale_f32_16x16x128_f8f6f4 v[118:121], v[172:179], v[204:211], v[118:121], v165, v165 op_sel_hi:[0,0,0]
	v_mfma_scale_f32_16x16x128_f8f6f4 v[110:113], v[2:9], v[212:219], v[110:113], v165, v165 op_sel_hi:[0,0,0]
	v_mfma_scale_f32_16x16x128_f8f6f4 v[102:105], v[172:179], v[212:219], v[102:105], v165, v165 op_sel_hi:[0,0,0]
	v_mfma_scale_f32_16x16x128_f8f6f4 v[94:97], v[2:9], v[220:227], v[94:97], v165, v165 op_sel_hi:[0,0,0]
	v_mfma_scale_f32_16x16x128_f8f6f4 v[86:89], v[172:179], v[220:227], v[86:89], v165, v165 op_sel_hi:[0,0,0]
	s_setprio 0
	s_setprio 1
	v_mfma_scale_f32_16x16x128_f8f6f4 v[138:141], v[180:187], v[196:203], v[138:141], v165, v165 op_sel_hi:[0,0,0]
	v_mfma_scale_f32_16x16x128_f8f6f4 v[130:133], v[188:195], v[196:203], v[130:133], v165, v165 op_sel_hi:[0,0,0]
	v_mfma_scale_f32_16x16x128_f8f6f4 v[122:125], v[180:187], v[204:211], v[122:125], v165, v165 op_sel_hi:[0,0,0]
	v_mfma_scale_f32_16x16x128_f8f6f4 v[114:117], v[188:195], v[204:211], v[114:117], v165, v165 op_sel_hi:[0,0,0]
	v_mfma_scale_f32_16x16x128_f8f6f4 v[106:109], v[180:187], v[212:219], v[106:109], v165, v165 op_sel_hi:[0,0,0]
	v_mfma_scale_f32_16x16x128_f8f6f4 v[98:101], v[188:195], v[212:219], v[98:101], v165, v165 op_sel_hi:[0,0,0]
	v_mfma_scale_f32_16x16x128_f8f6f4 v[90:93], v[180:187], v[220:227], v[90:93], v165, v165 op_sel_hi:[0,0,0]
	v_mfma_scale_f32_16x16x128_f8f6f4 v[82:85], v[188:195], v[220:227], v[82:85], v165, v165 op_sel_hi:[0,0,0]
	s_setprio 0
	s_barrier
; #define PG8_STAGE(bufoff, gbase, voff) do { _Pragma("unroll") for (int _i = 0; _i < 2; ++_i) \
;         __builtin_amdgcn_global_load_lds((const unsigned*)((const char*)(gbase) + (voff)[_i]), (LAS unsigned*)(lds + (bufoff) + ldsw + _i * 8192), 16, 0, 0); } while (0)
; #define PG8_LDA(dst, b, h) do { _Pragma("unroll") for (int m = 0; m < 4; ++m) { if constexpr (F8) dst##8[m] = PG8_LD32(lds + PG8_SA(b, h) + aoff + m * 2048); \
;         else { _Pragma("unroll") for (int k = 0; k < 2; ++k) dst[m][k] = *(const LAS bf16x8*)(lds + PG8_SA(b, h) + aoff + m * 2048 + k * 1024); } } } while (0)
; #define PG8_LDB(dst, b, h) do { _Pragma("unroll") for (int n = 0; n < 2; ++n) { if constexpr (F8) dst##8[n] = PG8_LD32(lds + PG8_SB(b, h) + boff + n * 2048); \
;         else { _Pragma("unroll") for (int k = 0; k < 2; ++k) dst[n][k] = *(const LAS bf16x8*)(lds + PG8_SB(b, h) + boff + n * 2048 + k * 1024); } } } while (0)
; #define PG8_WAIT_V(n) asm volatile("s_waitcnt vmcnt(" #n ")" ::: "memory")
; #define PG8_WAIT_L(n) asm volatile("s_waitcnt lgkmcnt(" #n ")" ::: "memory")
; #define PG8_BAR __builtin_amdgcn_s_barrier()
; #define PG8_SCHED __builtin_amdgcn_sched_barrier(0)
; template <class Epi, class Sched, bool GATHER, bool F8 = false>
; __device__ __forceinline__ void gemm_phase(LAS unsigned char* lds, const int K, const Sched& S, const Epi& E) {
;     ...
;             PG8_LDA(At, 0, 1); PG8_STAGE(PG8_SB(0, 0), b2, voffB); PG8_STAGE(PG8_SB(0, 1), b2 + hstepB, voffB); PG8_STAGE(PG8_SA(0, 0), a2, vN[0]);
;             PG8_WAIT_V(8); PG8_WAIT_L(0); PG8_BAR; PG8_MMA(1, 0, At, B0); PG8_MMA(1, 1, At, B1); PG8_BAR; PG8_SCHED;
;             PG8_LDB(B0, 1, 0); PG8_LDB(B1, 1, 1); PG8_SCHED; PG8_LDA(At, 1, 0); PG8_STAGE(PG8_SA(0, 1), a2, vN[1]);
	s_add_i32 s68, s58, s37
	v_lshl_add_u64 v[62:63], s[46:47], 0, v[148:149]
	s_mov_b32 m0, s68
	ds_read_b128 v[196:199], v168 offset:16384
	ds_read_b128 v[200:203], v168 offset:17408
	ds_read_b128 v[204:207], v168 offset:18432
	ds_read_b128 v[208:211], v168 offset:19456
	ds_read_b128 v[212:215], v168 offset:20480
	ds_read_b128 v[216:219], v168 offset:21504
	ds_read_b128 v[220:223], v168 offset:22528
	ds_read_b128 v[224:227], v168 offset:23552
	global_load_lds_dwordx4 v[62:63], off
	s_add_i32 m0, s68, 0x2000
	s_add_u32 s68, s46, 0x4000
	v_lshl_add_u64 v[64:65], s[46:47], 0, v[146:147]
	s_addc_u32 s69, s47, 0
	s_add_i32 s70, s59, s37
	global_load_lds_dwordx4 v[64:65], off
	v_lshl_add_u64 v[156:157], s[68:69], 0, v[148:149]
	s_mov_b32 m0, s70
	v_mov_b32_e32 v155, v153
	global_load_lds_dwordx4 v[156:157], off
	v_lshl_add_u64 v[156:157], s[68:69], 0, v[146:147]
	s_add_i32 m0, s70, 0x2000
	v_lshl_add_u64 v[158:159], s[48:49], 0, v[152:153]
	global_load_lds_dwordx4 v[156:157], off
	s_mov_b32 m0, s51
	v_lshl_add_u64 v[156:157], s[48:49], 0, v[154:155]
	global_load_lds_dwordx4 v152, s[48:49]
	s_mov_b32 m0, s52
	s_nop 0
	global_load_lds_dwordx4 v154, s[48:49]
	s_waitcnt vmcnt(8)
	s_waitcnt lgkmcnt(0)
	s_barrier
	s_setprio 1
	s_waitcnt lgkmcnt(0)
	v_mfma_scale_f32_16x16x128_f8f6f4 v[78:81], v[2:9], v[196:203], v[78:81], v165, v165 op_sel_hi:[0,0,0]
	v_mfma_scale_f32_16x16x128_f8f6f4 v[70:73], v[172:179], v[196:203], v[70:73], v165, v165 op_sel_hi:[0,0,0]
	v_mfma_scale_f32_16x16x128_f8f6f4 v[54:57], v[2:9], v[204:211], v[54:57], v165, v165 op_sel_hi:[0,0,0]
	v_mfma_scale_f32_16x16x128_f8f6f4 v[46:49], v[172:179], v[204:211], v[46:49], v165, v165 op_sel_hi:[0,0,0]
	v_mfma_scale_f32_16x16x128_f8f6f4 v[38:41], v[2:9], v[212:219], v[38:41], v165, v165 op_sel_hi:[0,0,0]
	v_mfma_scale_f32_16x16x128_f8f6f4 v[30:33], v[172:179], v[212:219], v[30:33], v165, v165 op_sel_hi:[0,0,0]
	v_mfma_scale_f32_16x16x128_f8f6f4 v[18:21], v[2:9], v[220:227], v[18:21], v165, v165 op_sel_hi:[0,0,0]
	v_mfma_scale_f32_16x16x128_f8f6f4 v[10:13], v[172:179], v[220:227], v[10:13], v165, v165 op_sel_hi:[0,0,0]
	s_setprio 0
	s_setprio 1
	v_mfma_scale_f32_16x16x128_f8f6f4 v[74:77], v[180:187], v[196:203], v[74:77], v165, v165 op_sel_hi:[0,0,0]
	v_mfma_scale_f32_16x16x128_f8f6f4 v[66:69], v[188:195], v[196:203], v[66:69], v165, v165 op_sel_hi:[0,0,0]
	v_mfma_scale_f32_16x16x128_f8f6f4 v[50:53], v[180:187], v[204:211], v[50:53], v165, v165 op_sel_hi:[0,0,0]
	v_mfma_scale_f32_16x16x128_f8f6f4 v[42:45], v[188:195], v[204:211], v[42:45], v165, v165 op_sel_hi:[0,0,0]
	v_mfma_scale_f32_16x16x128_f8f6f4 v[34:37], v[180:187], v[212:219], v[34:37], v165, v165 op_sel_hi:[0,0,0]
	v_mfma_scale_f32_16x16x128_f8f6f4 v[26:29], v[188:195], v[212:219], v[26:29], v165, v165 op_sel_hi:[0,0,0]
	v_mfma_scale_f32_16x16x128_f8f6f4 v[22:25], v[180:187], v[220:227], v[22:25], v165, v165 op_sel_hi:[0,0,0]
	v_mfma_scale_f32_16x16x128_f8f6f4 v[14:17], v[188:195], v[220:227], v[14:17], v165, v165 op_sel_hi:[0,0,0]
	s_setprio 0
	s_barrier
	s_add_i32 s68, 0, 0x18000
	s_add_i32 s69, 0, 0x1c000
	v_add_u32_e32 v2, s68, v167
	v_add_u32_e32 v155, s69, v167
	ds_read_b128 v[172:175], v2
	ds_read_b128 v[176:179], v2 offset:1024
	ds_read_b128 v[180:183], v2 offset:2048
	ds_read_b128 v[184:187], v2 offset:3072
	ds_read_b128 v[2:5], v155
	ds_read_b128 v[6:9], v155 offset:1024
	ds_read_b128 v[188:191], v155 offset:2048
	ds_read_b128 v[192:195], v155 offset:3072
	s_mov_b32 m0, s53
	ds_read_b128 v[196:199], v168 offset:32768
	ds_read_b128 v[200:203], v168 offset:33792
	ds_read_b128 v[204:207], v168 offset:34816
	ds_read_b128 v[208:211], v168 offset:35840
	ds_read_b128 v[212:215], v168 offset:36864
	ds_read_b128 v[216:219], v168 offset:37888
	ds_read_b128 v[220:223], v168 offset:38912
	ds_read_b128 v[224:227], v168 offset:39936
	global_load_lds_dwordx4 v163, s[48:49]
	s_mov_b32 m0, s54
	s_nop 0
	global_load_lds_dwordx4 v164, s[48:49]
	s_waitcnt vmcnt(8)
	s_waitcnt lgkmcnt(0)
	s_barrier
; #define PG8_STAGE(bufoff, gbase, voff) do { _Pragma("unroll") for (int _i = 0; _i < 2; ++_i) \
;         __builtin_amdgcn_global_load_lds((const unsigned*)((const char*)(gbase) + (voff)[_i]), (LAS unsigned*)(lds + (bufoff) + ldsw + _i * 8192), 16, 0, 0); } while (0)
; #define PG8_LDA(dst, b, h) do { _Pragma("unroll") for (int m = 0; m < 4; ++m) { if constexpr (F8) dst##8[m] = PG8_LD32(lds + PG8_SA(b, h) + aoff + m * 2048); \
;         else { _Pragma("unroll") for (int k = 0; k < 2; ++k) dst[m][k] = *(const LAS bf16x8*)(lds + PG8_SA(b, h) + aoff + m * 2048 + k * 1024); } } } while (0)
; #define PG8_WAIT_V(n) asm volatile("s_waitcnt vmcnt(" #n ")" ::: "memory")
; #define PG8_WAIT_L(n) asm volatile("s_waitcnt lgkmcnt(" #n ")" ::: "memory")
; #define PG8_BAR __builtin_amdgcn_s_barrier()
; #define PG8_SCHED __builtin_amdgcn_sched_barrier(0)
; template <class Epi, class Sched, bool GATHER, bool F8 = false>
; __device__ __forceinline__ void gemm_phase(LAS unsigned char* lds, const int K, const Sched& S, const Epi& E) {
;     ...
;             PG8_WAIT_V(8); PG8_WAIT_L(0); PG8_BAR; PG8_MMA(0, 0, At, B0); PG8_MMA(0, 1, At, B1); PG8_BAR; PG8_SCHED;
;             PG8_LDA(At, 1, 1); PG8_STAGE(PG8_SB(1, 0), b3, voffB); PG8_STAGE(PG8_SB(1, 1), b3 + hstepB, voffB); PG8_STAGE(PG8_SA(1, 0), a3, vN[0]);
;             PG8_WAIT_V(8); PG8_WAIT_L(0); PG8_BAR; PG8_MMA(1, 0, At, B0); PG8_MMA(1, 1, At, B1); PG8_BAR; PG8_SCHED;
;         }
	s_setprio 1
	s_waitcnt lgkmcnt(0)
	v_mfma_scale_f32_16x16x128_f8f6f4 v[142:145], v[172:179], v[196:203], v[142:145], v165, v165 op_sel_hi:[0,0,0]
	v_mfma_scale_f32_16x16x128_f8f6f4 v[134:137], v[180:187], v[196:203], v[134:137], v165, v165 op_sel_hi:[0,0,0]
	v_mfma_scale_f32_16x16x128_f8f6f4 v[126:129], v[172:179], v[204:211], v[126:129], v165, v165 op_sel_hi:[0,0,0]
	v_mfma_scale_f32_16x16x128_f8f6f4 v[118:121], v[180:187], v[204:211], v[118:121], v165, v165 op_sel_hi:[0,0,0]
	v_mfma_scale_f32_16x16x128_f8f6f4 v[110:113], v[172:179], v[212:219], v[110:113], v165, v165 op_sel_hi:[0,0,0]
	v_mfma_scale_f32_16x16x128_f8f6f4 v[102:105], v[180:187], v[212:219], v[102:105], v165, v165 op_sel_hi:[0,0,0]
	v_mfma_scale_f32_16x16x128_f8f6f4 v[94:97], v[172:179], v[220:227], v[94:97], v165, v165 op_sel_hi:[0,0,0]
	v_mfma_scale_f32_16x16x128_f8f6f4 v[86:89], v[180:187], v[220:227], v[86:89], v165, v165 op_sel_hi:[0,0,0]
	s_setprio 0
	s_setprio 1
	v_mfma_scale_f32_16x16x128_f8f6f4 v[138:141], v[2:9], v[196:203], v[138:141], v165, v165 op_sel_hi:[0,0,0]
	v_mfma_scale_f32_16x16x128_f8f6f4 v[130:133], v[188:195], v[196:203], v[130:133], v165, v165 op_sel_hi:[0,0,0]
	v_mfma_scale_f32_16x16x128_f8f6f4 v[122:125], v[2:9], v[204:211], v[122:125], v165, v165 op_sel_hi:[0,0,0]
	v_mfma_scale_f32_16x16x128_f8f6f4 v[114:117], v[188:195], v[204:211], v[114:117], v165, v165 op_sel_hi:[0,0,0]
	v_mfma_scale_f32_16x16x128_f8f6f4 v[106:109], v[2:9], v[212:219], v[106:109], v165, v165 op_sel_hi:[0,0,0]
	v_mfma_scale_f32_16x16x128_f8f6f4 v[98:101], v[188:195], v[212:219], v[98:101], v165, v165 op_sel_hi:[0,0,0]
	v_mfma_scale_f32_16x16x128_f8f6f4 v[90:93], v[2:9], v[220:227], v[90:93], v165, v165 op_sel_hi:[0,0,0]
	v_mfma_scale_f32_16x16x128_f8f6f4 v[82:85], v[188:195], v[220:227], v[82:85], v165, v165 op_sel_hi:[0,0,0]
	s_setprio 0
	s_barrier
	s_add_i32 s48, s68, s37
	v_lshl_add_u64 v[62:63], v[62:63], 0, s[100:101]
	s_mov_b32 m0, s48
	ds_read_b128 v[196:199], v168 offset:49152
	ds_read_b128 v[200:203], v168 offset:50176
	ds_read_b128 v[204:207], v168 offset:51200
	ds_read_b128 v[208:211], v168 offset:52224
	ds_read_b128 v[212:215], v168 offset:53248
	ds_read_b128 v[216:219], v168 offset:54272
	ds_read_b128 v[220:223], v168 offset:55296
	ds_read_b128 v[224:227], v168 offset:56320
	global_load_lds_dwordx4 v[62:63], off
	s_add_i32 m0, s48, 0x2000
	s_add_u32 s46, s46, 0xc000
	v_lshl_add_u64 v[62:63], v[64:65], 0, s[100:101]
	s_addc_u32 s47, s47, 0
	s_add_i32 s48, s69, s37
	global_load_lds_dwordx4 v[62:63], off
	v_lshl_add_u64 v[62:63], s[46:47], 0, v[148:149]
	s_mov_b32 m0, s48
	s_nop 0
	global_load_lds_dwordx4 v[62:63], off
	v_lshl_add_u64 v[62:63], s[46:47], 0, v[146:147]
	s_add_i32 m0, s48, 0x2000
	s_nop 0
	global_load_lds_dwordx4 v[62:63], off
	v_lshl_add_u64 v[62:63], v[158:159], 0, s[14:15]
	s_mov_b32 m0, s55
	s_nop 0
	global_load_lds_dwordx4 v[62:63], off
	v_lshl_add_u64 v[62:63], v[156:157], 0, s[14:15]
	s_mov_b32 m0, s56
	s_nop 0
	global_load_lds_dwordx4 v[62:63], off
	s_waitcnt vmcnt(8)
	s_waitcnt lgkmcnt(0)
	s_barrier
	s_setprio 1
	s_waitcnt lgkmcnt(0)
	v_mfma_scale_f32_16x16x128_f8f6f4 v[78:81], v[172:179], v[196:203], v[78:81], v165, v165 op_sel_hi:[0,0,0]
	v_mfma_scale_f32_16x16x128_f8f6f4 v[70:73], v[180:187], v[196:203], v[70:73], v165, v165 op_sel_hi:[0,0,0]
	v_mfma_scale_f32_16x16x128_f8f6f4 v[54:57], v[172:179], v[204:211], v[54:57], v165, v165 op_sel_hi:[0,0,0]
	v_mfma_scale_f32_16x16x128_f8f6f4 v[46:49], v[180:187], v[204:211], v[46:49], v165, v165 op_sel_hi:[0,0,0]
	v_mfma_scale_f32_16x16x128_f8f6f4 v[38:41], v[172:179], v[212:219], v[38:41], v165, v165 op_sel_hi:[0,0,0]
	v_mfma_scale_f32_16x16x128_f8f6f4 v[30:33], v[180:187], v[212:219], v[30:33], v165, v165 op_sel_hi:[0,0,0]
	v_mfma_scale_f32_16x16x128_f8f6f4 v[18:21], v[172:179], v[220:227], v[18:21], v165, v165 op_sel_hi:[0,0,0]
	v_mfma_scale_f32_16x16x128_f8f6f4 v[10:13], v[180:187], v[220:227], v[10:13], v165, v165 op_sel_hi:[0,0,0]
	s_setprio 0
	s_setprio 1
	v_mfma_scale_f32_16x16x128_f8f6f4 v[74:77], v[2:9], v[196:203], v[74:77], v165, v165 op_sel_hi:[0,0,0]
	v_mfma_scale_f32_16x16x128_f8f6f4 v[66:69], v[188:195], v[196:203], v[66:69], v165, v165 op_sel_hi:[0,0,0]
	v_mfma_scale_f32_16x16x128_f8f6f4 v[50:53], v[2:9], v[204:211], v[50:53], v165, v165 op_sel_hi:[0,0,0]
	v_mfma_scale_f32_16x16x128_f8f6f4 v[42:45], v[188:195], v[204:211], v[42:45], v165, v165 op_sel_hi:[0,0,0]
	v_mfma_scale_f32_16x16x128_f8f6f4 v[34:37], v[2:9], v[212:219], v[34:37], v165, v165 op_sel_hi:[0,0,0]
	v_mfma_scale_f32_16x16x128_f8f6f4 v[26:29], v[188:195], v[212:219], v[26:29], v165, v165 op_sel_hi:[0,0,0]
	v_mfma_scale_f32_16x16x128_f8f6f4 v[22:25], v[2:9], v[220:227], v[22:25], v165, v165 op_sel_hi:[0,0,0]
	v_mfma_scale_f32_16x16x128_f8f6f4 v[14:17], v[188:195], v[220:227], v[14:17], v165, v165 op_sel_hi:[0,0,0]
	s_setprio 0
	s_barrier
	s_add_i32 s67, s67, 2
	s_add_u32 s44, s44, 0x100
	s_addc_u32 s45, s45, 0
	s_add_u32 s65, s65, 0x10000
	s_addc_u32 s66, s66, 0
	s_cmp_gt_u32 s67, 13
	s_cbranch_scc1 .LBB0_1039

; #define PG8_STAGE(bufoff, gbase, voff) do { _Pragma("unroll") for (int _i = 0; _i < 2; ++_i) \
;         __builtin_amdgcn_global_load_lds((const unsigned*)((const char*)(gbase) + (voff)[_i]), (LAS unsigned*)(lds + (bufoff) + ldsw + _i * 8192), 16, 0, 0); } while (0)
; #define PG8_WAIT_V(n) asm volatile("s_waitcnt vmcnt(" #n ")" ::: "memory")
; #define PG8_BAR __builtin_amdgcn_s_barrier()
; template <class Epi, class Sched, bool GATHER, bool F8 = false>
; __device__ __forceinline__ void gemm_phase(LAS unsigned char* lds, const int K, const Sched& S, const Epi& E) {
;     ...
;     if constexpr (EpiInit<Epi>::value) { const typename EpiInit<Epi>::Pre p0 = E.preload(cur, wr, wc, fr, fq); E.init(acc, p0); }
;     int one_scale = 0x7f7f7f7f; asm volatile("" : "+v"(one_scale));
;     bf16x8 At[4][2], B0[2][2], B1[2][2]; i32x8 At8[4], B08[2], B18[2];
;     const char* cA = cur.A; const char* cB = cur.B;
;     PG8_STAGE(PG8_SB(0, 0), cB, voffB); PG8_STAGE(PG8_SB(0, 1), cB + hstepB, voffB); PG8_STAGE(PG8_SA(0, 0), cA, vA[0]); PG8_STAGE(PG8_SA(0, 1), cA, vA[1]);
;     if (wr == 1) PG8_BAR;
;     PG8_WAIT_V(2); PG8_BAR;
;     PG8_STAGE(PG8_SB(1, 0), cB + kstep, voffB); PG8_STAGE(PG8_SA(1, 0), cA + kstep, vA[0]); PG8_STAGE(PG8_SB(1, 1), cB + hstepB + kstep, voffB);
;     PG8_WAIT_V(6); PG8_BAR;
;     __device__ __forceinline__ bool next(int i, Unit& u) const {
;         const int x = c & 7, j = c >> 3, tile = 32 * i + 4 * x + (j & 3), pn = j >> 2;
;         if (tile >= tb.ntiles) return false;
;         const int e = tb.tile_e[tile];
;         u.A = H + (size_t)tile * 256 * DFF; u.B = W + ((size_t)e * DM + pn * 256) * DFF; u.row0 = tile * 256; u.col0 = pn * 256; u.tag = e; u.aux = 0; return true;
;     }
;     __device__ __forceinline__ Pre preload(const Unit& u, int wr, int wc, int fr, int fq) const {
;         const float* pb = bd + (size_t)u.tag * DM + u.col0 + wc * 64 + 8 * fq;
;         Pre p;
; #pragma unroll
;         for (int bj = 0; bj < 2; ++bj)
; #pragma unroll
;             for (int n = 0; n < 2; ++n) p.bv[bj][n] = *(const f32x4*)(pb + bj * 32 + 4 * n);
;         return p;
;     }
.LBB0_1119:
	s_add_i32 s0, 0, 0x20600
	v_mov_b32_e32 v1, s0
	ds_read_b32 v1, v1
	s_lshl_b32 s0, s2, 2
	s_and_b32 s0, s0, 28
	s_bfe_u32 s1, s2, 0x20003
	s_or_b32 s6, s0, s1
	s_waitcnt lgkmcnt(0)
	v_cmp_ge_i32_e32 vcc, s6, v1
	v_readfirstlane_b32 s20, v0
	s_cbranch_vccnz .LBB0_1135
	s_add_u32 s7, s82, 0x34000000
	s_addc_u32 s23, s83, 0
	s_add_u32 s18, s82, 0x24000000
	s_waitcnt vmcnt(0)
	v_lshlrev_b32_e32 v2, 4, v0
	s_addc_u32 s22, s83, 0
	s_lshr_b32 s0, s20, 6
	v_or_b32_e32 v18, 0x2000, v2
	v_and_b32_e32 v5, 32, v0
	s_lshl_b32 s25, s0, 10
	v_lshrrev_b32_e32 v3, 7, v18
	v_bfe_u32 v21, v0, 2, 4
	s_movk_i32 s0, 0x70
	v_bitop3_b32 v19, v2, v5, 48 bitop3:0x6c
	v_and_b32_e32 v20, 64, v0
	v_and_or_b32 v3, v3, s0, v21
	v_or_b32_e32 v2, v19, v20
	v_lshl_or_b32 v146, v3, 11, v2
	v_lshrrev_b32_e32 v3, 5, v0
	v_lshrrev_b32_e32 v6, 1, v0
	v_and_b32_e32 v3, 4, v3
	v_bfe_u32 v5, v0, 2, 2
	v_and_b32_e32 v6, 24, v6
	v_or3_b32 v3, v3, v5, v6
	v_lshrrev_b32_e32 v5, 6, v18
	s_movk_i32 s0, 0xc0
	v_and_or_b32 v5, v5, s0, v3
	s_lshl_b32 s0, s6, 2
	s_add_i32 s0, s0, 0
	s_add_i32 s0, s0, 0x20000
	v_mov_b32_e32 v6, s0
	ds_read_b32 v6, v6
	s_bfe_u32 s16, s20, 0x20006
	s_lshr_b32 s17, s20, 8
	s_lshl_b32 s0, s6, 19
	v_lshrrev_b32_e32 v4, 2, v0
	s_waitcnt lgkmcnt(0)
	v_readfirstlane_b32 s12, v6
	s_ashr_i32 s13, s12, 31
	s_add_u32 s44, s7, s0
	s_addc_u32 s45, s23, 0
	s_lshl_b32 s0, s2, 3
	s_and_b32 s0, s0, 0xffffff00
	s_ashr_i32 s1, s0, 31
	s_lshl_b64 s[2:3], s[12:13], 22
	s_lshl_b64 s[4:5], s[0:1], 11
	s_add_u32 s2, s18, s2
	s_addc_u32 s3, s22, s3
	s_add_u32 s46, s2, s4
	s_addc_u32 s47, s3, s5
	s_lshl_b64 s[2:3], s[12:13], 13
	s_add_u32 s13, s26, s2
	s_addc_u32 s14, s27, s3
	s_lshl_b64 s[2:3], s[0:1], 2
	s_add_u32 s1, s13, s2
	s_addc_u32 s3, s14, s3
	s_lshl_b32 s50, s16, 6
	s_lshl_b32 s2, s16, 8
	s_add_u32 s2, s1, s2
	v_bfe_u32 v22, v0, 4, 2
	v_lshl_or_b32 v150, v5, 11, v2
	v_lshrrev_b32_e32 v254, 11, v150
	v_and_b32_e32 v150, 0x7f, v150
	v_lshl_or_b32 v150, v254, 7, v150
	v_lshrrev_b32_e32 v5, 3, v0
	v_and_or_b32 v3, v4, 64, v3
	s_addc_u32 s3, s3, 0
	s_add_i32 s51, s25, 0
	v_and_or_b32 v5, v5, 48, v21
	v_lshl_or_b32 v156, v3, 11, v2
	v_lshrrev_b32_e32 v254, 11, v156
	v_and_b32_e32 v156, 0x7f, v156
	v_lshl_or_b32 v156, v254, 7, v156
	v_lshlrev_b32_e32 v10, 5, v22
	v_mov_b32_e32 v162, 0x7f7f7f7f
	s_add_i32 m0, s51, 0x10000
	v_lshl_or_b32 v152, v5, 11, v2
	global_load_dwordx4 v[74:77], v10, s[2:3] offset:16
	global_load_dwordx4 v[78:81], v10, s[2:3]
	global_load_dwordx4 v[2:5], v10, s[2:3] offset:144
	global_load_dwordx4 v[6:9], v10, s[2:3] offset:128
	global_load_lds_dwordx4 v156, s[46:47]
	s_add_i32 m0, s51, 0x12000
	s_add_u32 s2, s46, 0x1000
	global_load_lds_dwordx4 v150, s[46:47]
	s_addc_u32 s3, s47, 0
	s_add_i32 m0, s51, 0x14000
	s_add_i32 s52, s51, 0x2000
	global_load_lds_dwordx4 v156, s[2:3]
	s_add_i32 m0, s51, 0x16000
	s_add_i32 s53, s51, 0x4000
	global_load_lds_dwordx4 v150, s[2:3]
	s_mov_b32 m0, s51
	v_or_b32_e32 v154, 0x40000, v152
	global_load_lds_dwordx4 v152, s[44:45]
	s_mov_b32 m0, s52
	s_add_i32 s54, s51, 0x6000
	global_load_lds_dwordx4 v146, s[44:45]
	s_mov_b32 m0, s53
	v_or_b32_e32 v148, 0x40000, v146
	global_load_lds_dwordx4 v154, s[44:45]
	s_mov_b32 m0, s54
	v_mov_b32_e32 v157, 0
	global_load_lds_dwordx4 v148, s[44:45]
	v_mov_b32_e32 v151, v157
	v_mov_b32_e32 v153, v157
	v_mov_b32_e32 v147, v157
	s_cmp_eq_u32 s17, 1
	v_lshlrev_b32_e32 v23, 3, v22
	v_lshl_add_u64 v[16:17], s[46:47], 0, v[156:157]
	v_lshl_add_u64 v[14:15], s[46:47], 0, v[150:151]
	v_lshl_add_u64 v[10:11], s[44:45], 0, v[152:153]
	s_cselect_b64 s[2:3], -1, 0
	s_cmp_lg_u32 s17, 1
	v_lshl_add_u64 v[12:13], s[44:45], 0, v[146:147]
	s_cbranch_scc1 .LBB0_1122
	s_barrier
.LBB0_1122:
	s_lshl_b32 s64, s6, 8
	s_add_u32 s14, s82, 0x44600000
	s_addc_u32 s15, s83, 0
	s_lshl_b32 s55, s17, 6
	s_lshl_b32 s1, s17, 13
	s_lshl_b32 s13, s16, 12
	s_mov_b64 s[16:17], 0x80
	s_mov_b64 s[100:101], 0x8000
	s_add_i32 m0, s51, 0x18000
	v_lshl_add_u64 v[16:17], v[16:17], 0, s[100:101]
	s_waitcnt vmcnt(2)
	s_barrier
	global_load_lds_dwordx4 v[16:17], off
	v_lshl_add_u64 v[14:15], v[14:15], 0, s[100:101]
	s_add_i32 m0, s51, 0x1a000
	s_add_i32 s56, s51, 0x8000
	s_add_i32 s57, s51, 0xa000
	global_load_lds_dwordx4 v[14:15], off
	v_lshl_add_u64 v[10:11], v[10:11], 0, s[16:17]
	s_mov_b32 m0, s56
	s_add_u32 s36, s46, 0x9000
	global_load_lds_dwordx4 v[10:11], off
	v_lshl_add_u64 v[10:11], v[12:13], 0, s[16:17]
	s_mov_b32 m0, s57
	s_addc_u32 s37, s47, 0
	global_load_lds_dwordx4 v[10:11], off
	s_add_i32 m0, s51, 0x1c000
	v_lshl_add_u64 v[10:11], s[36:37], 0, v[156:157]
	global_load_lds_dwordx4 v[10:11], off
	v_lshl_add_u64 v[10:11], s[36:37], 0, v[150:151]
	s_add_i32 m0, s51, 0x1e000
	v_lshlrev_b32_e32 v13, 2, v0
	global_load_lds_dwordx4 v[10:11], off
	v_and_b32_e32 v10, 15, v0
	v_lshlrev_b32_e32 v11, 4, v22
	v_lshl_or_b32 v12, v10, 6, v11
	v_and_b32_e32 v13, 32, v13
	s_cmpk_lt_u32 s20, 0x100
	v_bitop3_b32 v12, v12, s1, v13 bitop3:0xde
	v_lshlrev_b32_e32 v14, 6, v0
	s_movk_i32 s1, 0x3c0
	s_cselect_b64 s[20:21], -1, 0
	s_add_u32 s58, s18, s4
	v_and_or_b32 v14, v14, s1, v11
	s_addc_u32 s59, s22, s5
	s_add_i32 s4, 0, 0x20800
	v_bitop3_b32 v163, s13, v14, v13 bitop3:0xf6
	v_lshrrev_b32_e32 v13, 6, v0
	s_movk_i32 s5, 0x900
	v_mov_b32_e32 v16, s4
	v_and_b32_e32 v14, 7, v0
	s_movk_i32 s1, 0x90
	v_mad_u32_u24 v13, v13, s5, v16
	v_lshl_or_b32 v164, v14, 3, s50
	v_mad_u32_u24 v10, v10, s1, v13
	v_lshl_add_u32 v13, v14, 4, v13
	v_lshlrev_b32_e32 v14, 8, v0
	v_and_b32_e32 v14, 0x18000, v14
	v_lshlrev_b32_e32 v16, 11, v21
	v_or3_b32 v14, v19, v14, v16
	v_add_u32_e32 v14, v14, v20
	v_or_b32_e32 v158, 0x40000, v14
	v_lshlrev_b32_e32 v14, 4, v18
	v_and_b32_e32 v14, 0x38000, v14
	s_waitcnt vmcnt(6)
	v_bfe_u32 v165, v0, 3, 3
	v_or3_b32 v14, v19, v14, v16
	v_mul_u32_u24_e32 v15, 0x90, v165
	v_add_u32_e32 v14, v14, v20
	v_mov_b32_e32 v155, v157
	v_mov_b32_e32 v149, v157
	s_mov_b32 s19, 0
	v_or_b32_e32 v166, 8, v165
	v_mov_b32_e32 v159, v157
	v_or_b32_e32 v160, 0x40000, v14
	v_mov_b32_e32 v161, v157
	s_mov_b32 s22, 0x42800000
	s_add_i32 s60, 0, 0x10000
	s_add_i32 s61, 0, 0x14000
	v_add_u32_e32 v167, 0, v12
	v_lshlrev_b32_e32 v168, 2, v23
	s_mov_b32 s24, 0x3c800000
	v_add_u32_e32 v169, v10, v11
	v_add_u32_e32 v171, v13, v15
	s_mov_b32 s62, 0
	s_barrier
	s_branch .LBB0_1125

; #define PG8_STAGE(bufoff, gbase, voff) do { _Pragma("unroll") for (int _i = 0; _i < 2; ++_i) \
;         __builtin_amdgcn_global_load_lds((const unsigned*)((const char*)(gbase) + (voff)[_i]), (LAS unsigned*)(lds + (bufoff) + ldsw + _i * 8192), 16, 0, 0); } while (0)
; #define PG8_LDA(dst, b, h) do { _Pragma("unroll") for (int m = 0; m < 4; ++m) { if constexpr (F8) dst##8[m] = PG8_LD32(lds + PG8_SA(b, h) + aoff + m * 2048); \
;         else { _Pragma("unroll") for (int k = 0; k < 2; ++k) dst[m][k] = *(const LAS bf16x8*)(lds + PG8_SA(b, h) + aoff + m * 2048 + k * 1024); } } } while (0)
; #define PG8_LDB(dst, b, h) do { _Pragma("unroll") for (int n = 0; n < 2; ++n) { if constexpr (F8) dst##8[n] = PG8_LD32(lds + PG8_SB(b, h) + boff + n * 2048); \
;         else { _Pragma("unroll") for (int k = 0; k < 2; ++k) dst[n][k] = *(const LAS bf16x8*)(lds + PG8_SB(b, h) + boff + n * 2048 + k * 1024); } } } while (0)
; #define PG8_WAIT_V(n) asm volatile("s_waitcnt vmcnt(" #n ")" ::: "memory")
; #define PG8_WAIT_L(n) asm volatile("s_waitcnt lgkmcnt(" #n ")" ::: "memory")
; #define PG8_BAR __builtin_amdgcn_s_barrier()
; #define PG8_SCHED __builtin_amdgcn_sched_barrier(0)
; template <class Epi, class Sched, bool GATHER, bool F8 = false>
; __device__ __forceinline__ void gemm_phase(LAS unsigned char* lds, const int K, const Sched& S, const Epi& E) {
;     ...
;             PG8_LDB(B0, 0, 0); PG8_LDB(B1, 0, 1); PG8_SCHED; PG8_LDA(At, 0, 0); PG8_STAGE(PG8_SA(1, 1), a1, vA[1]);
;             PG8_WAIT_V(8); PG8_WAIT_L(0); PG8_BAR; PG8_MMA(0, 0, At, B0); PG8_MMA(0, 1, At, B1); PG8_BAR; PG8_SCHED;
;     __device__ __forceinline__ void init(f32x4 (&acc)[2][2][4][2], const Pre& p) const {
; #pragma unroll
;         for (int ai = 0; ai < 2; ++ai)
; #pragma unroll
;             for (int bj = 0; bj < 2; ++bj)
; #pragma unroll
;                 for (int m = 0; m < 4; ++m)
; #pragma unroll
;                     for (int n = 0; n < 2; ++n) acc[ai][bj][m][n] = p.bv[bj][n] * WSCALE;
;     }
.LBB0_1127:
	s_add_u32 s44, s44, 0x80
	s_waitcnt vmcnt(0)
	v_pk_mul_f32 v[20:21], v[80:81], s[22:23] op_sel_hi:[1,0]
	v_pk_mul_f32 v[24:25], v[76:77], s[22:23] op_sel_hi:[1,0]
	v_pk_mul_f32 v[12:13], v[8:9], s[22:23] op_sel_hi:[1,0]
	v_pk_mul_f32 v[16:17], v[4:5], s[22:23] op_sel_hi:[1,0]
	s_addc_u32 s45, s45, 0
	v_pk_mul_f32 v[18:19], v[78:79], s[22:23] op_sel_hi:[1,0]
	v_pk_mul_f32 v[22:23], v[74:75], s[22:23] op_sel_hi:[1,0]
	v_pk_mul_f32 v[10:11], v[6:7], s[22:23] op_sel_hi:[1,0]
	v_pk_mul_f32 v[14:15], v[2:3], s[22:23] op_sel_hi:[1,0]
	s_add_u32 s1, s46, 0x10000
	v_mov_b64_e32 v[28:29], v[16:17]
	v_mov_b64_e32 v[32:33], v[12:13]
	v_mov_b64_e32 v[44:45], v[16:17]
	v_mov_b64_e32 v[48:49], v[12:13]
	v_mov_b64_e32 v[60:61], v[16:17]
	v_mov_b64_e32 v[64:65], v[12:13]
	v_mov_b64_e32 v[36:37], v[24:25]
	v_mov_b64_e32 v[40:41], v[20:21]
	v_mov_b64_e32 v[52:53], v[24:25]
	v_mov_b64_e32 v[56:57], v[20:21]
	v_mov_b64_e32 v[68:69], v[24:25]
	v_mov_b64_e32 v[72:73], v[20:21]
	v_mov_b64_e32 v[84:85], v[16:17]
	v_mov_b64_e32 v[88:89], v[12:13]
	v_mov_b64_e32 v[100:101], v[16:17]
	v_mov_b64_e32 v[104:105], v[12:13]
	v_mov_b64_e32 v[116:117], v[16:17]
	v_mov_b64_e32 v[120:121], v[12:13]
	v_mov_b64_e32 v[132:133], v[16:17]
	v_mov_b64_e32 v[136:137], v[12:13]
	v_mov_b64_e32 v[92:93], v[24:25]
	v_mov_b64_e32 v[96:97], v[20:21]
	v_mov_b64_e32 v[108:109], v[24:25]
	v_mov_b64_e32 v[112:113], v[20:21]
	v_mov_b64_e32 v[124:125], v[24:25]
	v_mov_b64_e32 v[128:129], v[20:21]
	v_mov_b64_e32 v[140:141], v[24:25]
	v_mov_b64_e32 v[144:145], v[20:21]
	s_addc_u32 s13, s47, 0
	s_mov_b32 s18, -2
	v_mov_b64_e32 v[26:27], v[14:15]
	v_mov_b64_e32 v[30:31], v[10:11]
	v_mov_b64_e32 v[42:43], v[14:15]
	v_mov_b64_e32 v[46:47], v[10:11]
	v_mov_b64_e32 v[58:59], v[14:15]
	v_mov_b64_e32 v[62:63], v[10:11]
	v_mov_b64_e32 v[34:35], v[22:23]
	v_mov_b64_e32 v[38:39], v[18:19]
	v_mov_b64_e32 v[50:51], v[22:23]
	v_mov_b64_e32 v[54:55], v[18:19]
	v_mov_b64_e32 v[66:67], v[22:23]
	v_mov_b64_e32 v[70:71], v[18:19]
	v_mov_b64_e32 v[82:83], v[14:15]
	v_mov_b64_e32 v[86:87], v[10:11]
	v_mov_b64_e32 v[98:99], v[14:15]
	v_mov_b64_e32 v[102:103], v[10:11]
	v_mov_b64_e32 v[114:115], v[14:15]
	v_mov_b64_e32 v[118:119], v[10:11]
	v_mov_b64_e32 v[130:131], v[14:15]
	v_mov_b64_e32 v[134:135], v[10:11]
	v_mov_b64_e32 v[90:91], v[22:23]
	v_mov_b64_e32 v[94:95], v[18:19]
	v_mov_b64_e32 v[106:107], v[22:23]
	v_mov_b64_e32 v[110:111], v[18:19]
	v_mov_b64_e32 v[122:123], v[22:23]
	v_mov_b64_e32 v[126:127], v[18:19]
	v_mov_b64_e32 v[138:139], v[22:23]
	v_mov_b64_e32 v[142:143], v[18:19]
.LBB0_1128:
	v_add_u32_e32 v74, s60, v163
	ds_read_b128 v[2:5], v74
	ds_read_b128 v[6:9], v74 offset:1024
	ds_read_b128 v[172:175], v74 offset:2048
	ds_read_b128 v[176:179], v74 offset:3072
	v_add_u32_e32 v74, s61, v163
	ds_read_b128 v[180:183], v74
	ds_read_b128 v[184:187], v74 offset:1024
	ds_read_b128 v[188:191], v74 offset:2048
	ds_read_b128 v[192:195], v74 offset:3072
	s_add_u32 s46, s44, 0x80
	s_addc_u32 s47, s45, 0
	s_cmp_eq_u32 s18, 12
	s_cselect_b32 s49, s41, s47
	s_cselect_b32 s48, s40, s46
	s_cselect_b32 s47, s43, s13
	s_cselect_b32 s46, s42, s1
	v_lshl_add_u64 v[220:221], s[44:45], 0, v[158:159]
	s_add_i32 m0, s51, 0xc000
	ds_read_b128 v[74:77], v167
	ds_read_b128 v[78:81], v167 offset:1024
	ds_read_b128 v[196:199], v167 offset:2048
	ds_read_b128 v[200:203], v167 offset:3072
	ds_read_b128 v[204:207], v167 offset:4096
	ds_read_b128 v[208:211], v167 offset:5120
	ds_read_b128 v[212:215], v167 offset:6144
	ds_read_b128 v[216:219], v167 offset:7168
	global_load_lds_dwordx4 v[220:221], off
	v_lshl_add_u64 v[220:221], s[44:45], 0, v[160:161]
	s_add_i32 m0, s51, 0xe000
	s_nop 0
	global_load_lds_dwordx4 v[220:221], off
	s_waitcnt vmcnt(8)
	s_waitcnt lgkmcnt(0)
	s_barrier
	s_setprio 1
	s_waitcnt lgkmcnt(0)
	v_mfma_scale_f32_16x16x128_f8f6f4 v[142:145], v[2:9], v[74:81], v[142:145], v162, v162 op_sel_hi:[0,0,0]
	v_mfma_scale_f32_16x16x128_f8f6f4 v[138:141], v[172:179], v[74:81], v[138:141], v162, v162 op_sel_hi:[0,0,0]
	v_mfma_scale_f32_16x16x128_f8f6f4 v[126:129], v[2:9], v[196:203], v[126:129], v162, v162 op_sel_hi:[0,0,0]
	v_mfma_scale_f32_16x16x128_f8f6f4 v[122:125], v[172:179], v[196:203], v[122:125], v162, v162 op_sel_hi:[0,0,0]
	v_mfma_scale_f32_16x16x128_f8f6f4 v[110:113], v[2:9], v[204:211], v[110:113], v162, v162 op_sel_hi:[0,0,0]
	v_mfma_scale_f32_16x16x128_f8f6f4 v[106:109], v[172:179], v[204:211], v[106:109], v162, v162 op_sel_hi:[0,0,0]
	v_mfma_scale_f32_16x16x128_f8f6f4 v[94:97], v[2:9], v[212:219], v[94:97], v162, v162 op_sel_hi:[0,0,0]
	v_mfma_scale_f32_16x16x128_f8f6f4 v[90:93], v[172:179], v[212:219], v[90:93], v162, v162 op_sel_hi:[0,0,0]
	s_setprio 0
	s_setprio 1
	v_mfma_scale_f32_16x16x128_f8f6f4 v[134:137], v[180:187], v[74:81], v[134:137], v162, v162 op_sel_hi:[0,0,0]
	v_mfma_scale_f32_16x16x128_f8f6f4 v[130:133], v[188:195], v[74:81], v[130:133], v162, v162 op_sel_hi:[0,0,0]
	v_mfma_scale_f32_16x16x128_f8f6f4 v[118:121], v[180:187], v[196:203], v[118:121], v162, v162 op_sel_hi:[0,0,0]
	v_mfma_scale_f32_16x16x128_f8f6f4 v[114:117], v[188:195], v[196:203], v[114:117], v162, v162 op_sel_hi:[0,0,0]
	v_mfma_scale_f32_16x16x128_f8f6f4 v[102:105], v[180:187], v[204:211], v[102:105], v162, v162 op_sel_hi:[0,0,0]
	v_mfma_scale_f32_16x16x128_f8f6f4 v[98:101], v[188:195], v[204:211], v[98:101], v162, v162 op_sel_hi:[0,0,0]
	v_mfma_scale_f32_16x16x128_f8f6f4 v[86:89], v[180:187], v[212:219], v[86:89], v162, v162 op_sel_hi:[0,0,0]
	v_mfma_scale_f32_16x16x128_f8f6f4 v[82:85], v[188:195], v[212:219], v[82:85], v162, v162 op_sel_hi:[0,0,0]
	s_setprio 0
	s_barrier
; #define PG8_STAGE(bufoff, gbase, voff) do { _Pragma("unroll") for (int _i = 0; _i < 2; ++_i) \
;         __builtin_amdgcn_global_load_lds((const unsigned*)((const char*)(gbase) + (voff)[_i]), (LAS unsigned*)(lds + (bufoff) + ldsw + _i * 8192), 16, 0, 0); } while (0)
; #define PG8_LDA(dst, b, h) do { _Pragma("unroll") for (int m = 0; m < 4; ++m) { if constexpr (F8) dst##8[m] = PG8_LD32(lds + PG8_SA(b, h) + aoff + m * 2048); \
;         else { _Pragma("unroll") for (int k = 0; k < 2; ++k) dst[m][k] = *(const LAS bf16x8*)(lds + PG8_SA(b, h) + aoff + m * 2048 + k * 1024); } } } while (0)
; #define PG8_LDB(dst, b, h) do { _Pragma("unroll") for (int n = 0; n < 2; ++n) { if constexpr (F8) dst##8[n] = PG8_LD32(lds + PG8_SB(b, h) + boff + n * 2048); \
;         else { _Pragma("unroll") for (int k = 0; k < 2; ++k) dst[n][k] = *(const LAS bf16x8*)(lds + PG8_SB(b, h) + boff + n * 2048 + k * 1024); } } } while (0)
; #define PG8_WAIT_V(n) asm volatile("s_waitcnt vmcnt(" #n ")" ::: "memory")
; #define PG8_WAIT_L(n) asm volatile("s_waitcnt lgkmcnt(" #n ")" ::: "memory")
; #define PG8_BAR __builtin_amdgcn_s_barrier()
; #define PG8_SCHED __builtin_amdgcn_sched_barrier(0)
; template <class Epi, class Sched, bool GATHER, bool F8 = false>
; __device__ __forceinline__ void gemm_phase(LAS unsigned char* lds, const int K, const Sched& S, const Epi& E) {
;     ...
;             PG8_LDA(At, 0, 1); PG8_STAGE(PG8_SB(0, 0), b2, voffB); PG8_STAGE(PG8_SB(0, 1), b2 + hstepB, voffB); PG8_STAGE(PG8_SA(0, 0), a2, vN[0]);
;             PG8_WAIT_V(8); PG8_WAIT_L(0); PG8_BAR; PG8_MMA(1, 0, At, B0); PG8_MMA(1, 1, At, B1); PG8_BAR; PG8_SCHED;
;             PG8_LDB(B0, 1, 0); PG8_LDB(B1, 1, 1); PG8_SCHED; PG8_LDA(At, 1, 0); PG8_STAGE(PG8_SA(0, 1), a2, vN[1]);
	s_add_i32 s65, s60, s25
	v_lshl_add_u64 v[74:75], s[46:47], 0, v[156:157]
	s_mov_b32 m0, s65
	ds_read_b128 v[196:199], v167 offset:16384
	ds_read_b128 v[200:203], v167 offset:17408
	ds_read_b128 v[204:207], v167 offset:18432
	ds_read_b128 v[208:211], v167 offset:19456
	ds_read_b128 v[212:215], v167 offset:20480
	ds_read_b128 v[216:219], v167 offset:21504
	ds_read_b128 v[220:223], v167 offset:22528
	ds_read_b128 v[224:227], v167 offset:23552
	global_load_lds_dwordx4 v[74:75], off
	s_add_i32 m0, s65, 0x2000
	s_add_u32 s66, s46, 0x1000
	v_lshl_add_u64 v[76:77], s[46:47], 0, v[150:151]
	s_addc_u32 s67, s47, 0
	s_add_i32 s65, s61, s25
	global_load_lds_dwordx4 v[76:77], off
	v_lshl_add_u64 v[78:79], s[66:67], 0, v[156:157]
	s_mov_b32 m0, s65
	v_lshl_add_u64 v[80:81], s[48:49], 0, v[146:147]
	global_load_lds_dwordx4 v[78:79], off
	v_lshl_add_u64 v[78:79], s[66:67], 0, v[150:151]
	s_add_i32 m0, s65, 0x2000
	s_nop 0
	global_load_lds_dwordx4 v[78:79], off
	v_lshl_add_u64 v[78:79], s[48:49], 0, v[152:153]
	s_mov_b32 m0, s51
	s_nop 0
	global_load_lds_dwordx4 v[78:79], off
	s_mov_b32 m0, s52
	s_nop 0
	global_load_lds_dwordx4 v[80:81], off
	s_waitcnt vmcnt(8)
	s_waitcnt lgkmcnt(0)
	s_barrier
	s_setprio 1
	s_waitcnt lgkmcnt(0)
	v_mfma_scale_f32_16x16x128_f8f6f4 v[70:73], v[2:9], v[196:203], v[70:73], v162, v162 op_sel_hi:[0,0,0]
	v_mfma_scale_f32_16x16x128_f8f6f4 v[66:69], v[172:179], v[196:203], v[66:69], v162, v162 op_sel_hi:[0,0,0]
	v_mfma_scale_f32_16x16x128_f8f6f4 v[54:57], v[2:9], v[204:211], v[54:57], v162, v162 op_sel_hi:[0,0,0]
	v_mfma_scale_f32_16x16x128_f8f6f4 v[50:53], v[172:179], v[204:211], v[50:53], v162, v162 op_sel_hi:[0,0,0]
	v_mfma_scale_f32_16x16x128_f8f6f4 v[38:41], v[2:9], v[212:219], v[38:41], v162, v162 op_sel_hi:[0,0,0]
	v_mfma_scale_f32_16x16x128_f8f6f4 v[34:37], v[172:179], v[212:219], v[34:37], v162, v162 op_sel_hi:[0,0,0]
	v_mfma_scale_f32_16x16x128_f8f6f4 v[18:21], v[2:9], v[220:227], v[18:21], v162, v162 op_sel_hi:[0,0,0]
	v_mfma_scale_f32_16x16x128_f8f6f4 v[22:25], v[172:179], v[220:227], v[22:25], v162, v162 op_sel_hi:[0,0,0]
	s_setprio 0
	s_setprio 1
	v_mfma_scale_f32_16x16x128_f8f6f4 v[62:65], v[180:187], v[196:203], v[62:65], v162, v162 op_sel_hi:[0,0,0]
	v_mfma_scale_f32_16x16x128_f8f6f4 v[58:61], v[188:195], v[196:203], v[58:61], v162, v162 op_sel_hi:[0,0,0]
	v_mfma_scale_f32_16x16x128_f8f6f4 v[46:49], v[180:187], v[204:211], v[46:49], v162, v162 op_sel_hi:[0,0,0]
	v_mfma_scale_f32_16x16x128_f8f6f4 v[42:45], v[188:195], v[204:211], v[42:45], v162, v162 op_sel_hi:[0,0,0]
	v_mfma_scale_f32_16x16x128_f8f6f4 v[30:33], v[180:187], v[212:219], v[30:33], v162, v162 op_sel_hi:[0,0,0]
	v_mfma_scale_f32_16x16x128_f8f6f4 v[26:29], v[188:195], v[212:219], v[26:29], v162, v162 op_sel_hi:[0,0,0]
	v_mfma_scale_f32_16x16x128_f8f6f4 v[10:13], v[180:187], v[220:227], v[10:13], v162, v162 op_sel_hi:[0,0,0]
	v_mfma_scale_f32_16x16x128_f8f6f4 v[14:17], v[188:195], v[220:227], v[14:17], v162, v162 op_sel_hi:[0,0,0]
	s_setprio 0
	s_barrier
	s_add_i32 s65, 0, 0x18000
	s_add_i32 s66, 0, 0x1c000
	v_add_u32_e32 v2, s65, v163
	v_add_u32_e32 v192, s66, v163
	ds_read_b128 v[172:175], v2
	ds_read_b128 v[176:179], v2 offset:1024
	ds_read_b128 v[180:183], v2 offset:2048
	ds_read_b128 v[184:187], v2 offset:3072
	ds_read_b128 v[2:5], v192
	ds_read_b128 v[6:9], v192 offset:1024
	ds_read_b128 v[188:191], v192 offset:2048
	ds_read_b128 v[192:195], v192 offset:3072
	s_mov_b32 m0, s53
	v_lshl_add_u64 v[228:229], s[48:49], 0, v[154:155]
	ds_read_b128 v[196:199], v167 offset:32768
	ds_read_b128 v[200:203], v167 offset:33792
	ds_read_b128 v[204:207], v167 offset:34816
	ds_read_b128 v[208:211], v167 offset:35840
	ds_read_b128 v[212:215], v167 offset:36864
	ds_read_b128 v[216:219], v167 offset:37888
	ds_read_b128 v[220:223], v167 offset:38912
	ds_read_b128 v[224:227], v167 offset:39936
	global_load_lds_dwordx4 v[228:229], off
	v_lshl_add_u64 v[228:229], s[48:49], 0, v[148:149]
	s_mov_b32 m0, s54
	s_nop 0
	global_load_lds_dwordx4 v[228:229], off
	s_waitcnt vmcnt(8)
	s_waitcnt lgkmcnt(0)
	s_barrier
; #define PG8_STAGE(bufoff, gbase, voff) do { _Pragma("unroll") for (int _i = 0; _i < 2; ++_i) \
;         __builtin_amdgcn_global_load_lds((const unsigned*)((const char*)(gbase) + (voff)[_i]), (LAS unsigned*)(lds + (bufoff) + ldsw + _i * 8192), 16, 0, 0); } while (0)
; #define PG8_LDA(dst, b, h) do { _Pragma("unroll") for (int m = 0; m < 4; ++m) { if constexpr (F8) dst##8[m] = PG8_LD32(lds + PG8_SA(b, h) + aoff + m * 2048); \
;         else { _Pragma("unroll") for (int k = 0; k < 2; ++k) dst[m][k] = *(const LAS bf16x8*)(lds + PG8_SA(b, h) + aoff + m * 2048 + k * 1024); } } } while (0)
; #define PG8_WAIT_V(n) asm volatile("s_waitcnt vmcnt(" #n ")" ::: "memory")
; #define PG8_WAIT_L(n) asm volatile("s_waitcnt lgkmcnt(" #n ")" ::: "memory")
; #define PG8_BAR __builtin_amdgcn_s_barrier()
; #define PG8_SCHED __builtin_amdgcn_sched_barrier(0)
; template <class Epi, class Sched, bool GATHER, bool F8 = false>
; __device__ __forceinline__ void gemm_phase(LAS unsigned char* lds, const int K, const Sched& S, const Epi& E) {
;     ...
;             PG8_WAIT_V(8); PG8_WAIT_L(0); PG8_BAR; PG8_MMA(0, 0, At, B0); PG8_MMA(0, 1, At, B1); PG8_BAR; PG8_SCHED;
;             PG8_LDA(At, 1, 1); PG8_STAGE(PG8_SB(1, 0), b3, voffB); PG8_STAGE(PG8_SB(1, 1), b3 + hstepB, voffB); PG8_STAGE(PG8_SA(1, 0), a3, vN[0]);
;             PG8_WAIT_V(8); PG8_WAIT_L(0); PG8_BAR; PG8_MMA(1, 0, At, B0); PG8_MMA(1, 1, At, B1); PG8_BAR; PG8_SCHED;
;         }
;         if (wr == 0) PG8_BAR;
	s_setprio 1
	s_waitcnt lgkmcnt(0)
	v_mfma_scale_f32_16x16x128_f8f6f4 v[142:145], v[172:179], v[196:203], v[142:145], v162, v162 op_sel_hi:[0,0,0]
	v_mfma_scale_f32_16x16x128_f8f6f4 v[138:141], v[180:187], v[196:203], v[138:141], v162, v162 op_sel_hi:[0,0,0]
	v_mfma_scale_f32_16x16x128_f8f6f4 v[126:129], v[172:179], v[204:211], v[126:129], v162, v162 op_sel_hi:[0,0,0]
	v_mfma_scale_f32_16x16x128_f8f6f4 v[122:125], v[180:187], v[204:211], v[122:125], v162, v162 op_sel_hi:[0,0,0]
	v_mfma_scale_f32_16x16x128_f8f6f4 v[110:113], v[172:179], v[212:219], v[110:113], v162, v162 op_sel_hi:[0,0,0]
	v_mfma_scale_f32_16x16x128_f8f6f4 v[106:109], v[180:187], v[212:219], v[106:109], v162, v162 op_sel_hi:[0,0,0]
	v_mfma_scale_f32_16x16x128_f8f6f4 v[94:97], v[172:179], v[220:227], v[94:97], v162, v162 op_sel_hi:[0,0,0]
	v_mfma_scale_f32_16x16x128_f8f6f4 v[90:93], v[180:187], v[220:227], v[90:93], v162, v162 op_sel_hi:[0,0,0]
	s_setprio 0
	s_setprio 1
	v_mfma_scale_f32_16x16x128_f8f6f4 v[134:137], v[2:9], v[196:203], v[134:137], v162, v162 op_sel_hi:[0,0,0]
	v_mfma_scale_f32_16x16x128_f8f6f4 v[130:133], v[188:195], v[196:203], v[130:133], v162, v162 op_sel_hi:[0,0,0]
	v_mfma_scale_f32_16x16x128_f8f6f4 v[118:121], v[2:9], v[204:211], v[118:121], v162, v162 op_sel_hi:[0,0,0]
	v_mfma_scale_f32_16x16x128_f8f6f4 v[114:117], v[188:195], v[204:211], v[114:117], v162, v162 op_sel_hi:[0,0,0]
	v_mfma_scale_f32_16x16x128_f8f6f4 v[102:105], v[2:9], v[212:219], v[102:105], v162, v162 op_sel_hi:[0,0,0]
	v_mfma_scale_f32_16x16x128_f8f6f4 v[98:101], v[188:195], v[212:219], v[98:101], v162, v162 op_sel_hi:[0,0,0]
	v_mfma_scale_f32_16x16x128_f8f6f4 v[86:89], v[2:9], v[220:227], v[86:89], v162, v162 op_sel_hi:[0,0,0]
	v_mfma_scale_f32_16x16x128_f8f6f4 v[82:85], v[188:195], v[220:227], v[82:85], v162, v162 op_sel_hi:[0,0,0]
	s_setprio 0
	s_barrier
	s_add_i32 s48, s65, s25
	v_lshl_add_u64 v[74:75], v[74:75], 0, s[100:101]
	s_mov_b32 m0, s48
	ds_read_b128 v[196:199], v167 offset:49152
	ds_read_b128 v[200:203], v167 offset:50176
	ds_read_b128 v[204:207], v167 offset:51200
	ds_read_b128 v[208:211], v167 offset:52224
	ds_read_b128 v[212:215], v167 offset:53248
	ds_read_b128 v[216:219], v167 offset:54272
	ds_read_b128 v[220:223], v167 offset:55296
	ds_read_b128 v[224:227], v167 offset:56320
	global_load_lds_dwordx4 v[74:75], off
	s_add_i32 m0, s48, 0x2000
	s_add_u32 s46, s46, 0x9000
	v_lshl_add_u64 v[74:75], v[76:77], 0, s[100:101]
	s_addc_u32 s47, s47, 0
	s_add_i32 s48, s66, s25
	global_load_lds_dwordx4 v[74:75], off
	v_lshl_add_u64 v[74:75], s[46:47], 0, v[156:157]
	s_mov_b32 m0, s48
	s_nop 0
	global_load_lds_dwordx4 v[74:75], off
	v_lshl_add_u64 v[74:75], s[46:47], 0, v[150:151]
	s_add_i32 m0, s48, 0x2000
	s_nop 0
	global_load_lds_dwordx4 v[74:75], off
	v_lshl_add_u64 v[74:75], v[78:79], 0, s[16:17]
	s_mov_b32 m0, s56
	s_nop 0
	global_load_lds_dwordx4 v[74:75], off
	v_lshl_add_u64 v[74:75], v[80:81], 0, s[16:17]
	s_mov_b32 m0, s57
	s_nop 0
	global_load_lds_dwordx4 v[74:75], off
	s_waitcnt vmcnt(8)
	s_waitcnt lgkmcnt(0)
	s_barrier
	s_setprio 1
	s_waitcnt lgkmcnt(0)
	v_mfma_scale_f32_16x16x128_f8f6f4 v[70:73], v[172:179], v[196:203], v[70:73], v162, v162 op_sel_hi:[0,0,0]
	v_mfma_scale_f32_16x16x128_f8f6f4 v[66:69], v[180:187], v[196:203], v[66:69], v162, v162 op_sel_hi:[0,0,0]
	v_mfma_scale_f32_16x16x128_f8f6f4 v[54:57], v[172:179], v[204:211], v[54:57], v162, v162 op_sel_hi:[0,0,0]
	v_mfma_scale_f32_16x16x128_f8f6f4 v[50:53], v[180:187], v[204:211], v[50:53], v162, v162 op_sel_hi:[0,0,0]
	v_mfma_scale_f32_16x16x128_f8f6f4 v[38:41], v[172:179], v[212:219], v[38:41], v162, v162 op_sel_hi:[0,0,0]
	v_mfma_scale_f32_16x16x128_f8f6f4 v[34:37], v[180:187], v[212:219], v[34:37], v162, v162 op_sel_hi:[0,0,0]
	v_mfma_scale_f32_16x16x128_f8f6f4 v[18:21], v[172:179], v[220:227], v[18:21], v162, v162 op_sel_hi:[0,0,0]
	v_mfma_scale_f32_16x16x128_f8f6f4 v[22:25], v[180:187], v[220:227], v[22:25], v162, v162 op_sel_hi:[0,0,0]
	s_setprio 0
	s_setprio 1
	v_mfma_scale_f32_16x16x128_f8f6f4 v[62:65], v[2:9], v[196:203], v[62:65], v162, v162 op_sel_hi:[0,0,0]
	v_mfma_scale_f32_16x16x128_f8f6f4 v[58:61], v[188:195], v[196:203], v[58:61], v162, v162 op_sel_hi:[0,0,0]
	v_mfma_scale_f32_16x16x128_f8f6f4 v[46:49], v[2:9], v[204:211], v[46:49], v162, v162 op_sel_hi:[0,0,0]
	v_mfma_scale_f32_16x16x128_f8f6f4 v[42:45], v[188:195], v[204:211], v[42:45], v162, v162 op_sel_hi:[0,0,0]
	v_mfma_scale_f32_16x16x128_f8f6f4 v[30:33], v[2:9], v[212:219], v[30:33], v162, v162 op_sel_hi:[0,0,0]
	v_mfma_scale_f32_16x16x128_f8f6f4 v[26:29], v[188:195], v[212:219], v[26:29], v162, v162 op_sel_hi:[0,0,0]
	v_mfma_scale_f32_16x16x128_f8f6f4 v[10:13], v[2:9], v[220:227], v[10:13], v162, v162 op_sel_hi:[0,0,0]
	v_mfma_scale_f32_16x16x128_f8f6f4 v[14:17], v[188:195], v[220:227], v[14:17], v162, v162 op_sel_hi:[0,0,0]
	s_setprio 0
	s_barrier
	s_add_i32 s18, s18, 2
	s_add_u32 s44, s44, 0x100
	s_addc_u32 s45, s45, 0
	s_add_u32 s1, s1, 0x10000
	s_addc_u32 s13, s13, 0
	s_cmp_gt_u32 s18, 13
	s_cbranch_scc0 .LBB0_1128
	s_and_b64 vcc, exec, s[20:21]
	s_cbranch_vccz .LBB0_1131
	s_barrier
